# v25 plus: in the GEMM K-loops the per-phase s_setprio 1 is issued before (not after) the barrier that opens each MFMA segment
# speedup vs baseline: 1.0129x; 1.0129x over previous
; #define PG8_STAGE(bufoff, gbase, voff) do { _Pragma("unroll") for (int _i = 0; _i < 2; ++_i) \
;         __builtin_amdgcn_global_load_lds((const unsigned*)((const char*)(gbase) + (voff)[_i]), (PG8_LAS unsigned*)(lds + (bufoff) + ldsw + _i * 8192), 16, 0, 0); } while (0)
; #define PG8_LDA(dst, b, h) do { _Pragma("unroll") for (int m = 0; m < 4; ++m) _Pragma("unroll") for (int k = 0; k < 2; ++k) dst[m][k] = *(const PG8_LAS bf16x8*)(lds + PG8_SA(b, h) + aoff + m * 2048 + k * 1024); } while (0)
; #define PG8_LDB(dst, b, h) do { _Pragma("unroll") for (int n = 0; n < 2; ++n) _Pragma("unroll") for (int k = 0; k < 2; ++k) dst[n][k] = *(const PG8_LAS bf16x8*)(lds + PG8_SB(b, h) + boff + n * 2048 + k * 1024); } while (0)
; #define PG8_WAIT_V(n) asm volatile("s_waitcnt vmcnt(" #n ")" ::: "memory")
; #define PG8_WAIT_L(n) asm volatile("s_waitcnt lgkmcnt(" #n ")" ::: "memory")
; #define PG8_BAR __builtin_amdgcn_s_barrier()
; #define PG8_SCHED __builtin_amdgcn_sched_barrier(0)
; template <class Epi, class Sched, bool ALIGN_EPI = false, bool SP2 = false, bool FP8 = false>
; __device__ __forceinline__ void gemm_phase(PG8_LAS unsigned char* lds, const Gemm g, const Sched& S, const Epi& E) {
;     ...
;             const bool last = (t == nt - 2);
;             const char* a1 = cA + (size_t)(t + 1) * kstep;
;             const char* a2 = last ? nA : cA + (size_t)(t + 2) * kstep; const char* b2 = last ? nB : cB + (size_t)(t + 2) * kstep;
;             const char* a3 = a2 + kstep; const char* b3 = b2 + kstep;
;             if (last && has_next) S.a_ready(nxt);
;             if constexpr (SP2) {
;             PG8_LDB(B0, 0, 0); PG8_LDB(B1, 0, 1); PG8_SCHED; PG8_LDA(At, 0, 0); PG8_STAGE(PG8_SA(1, 1), a1 + hstep, voffA);
;             PG8_WAIT_V(8); PG8_WAIT_L(0); PG8_BAR; PG8_MMA(0, 0, At, B0); PG8_MMA(0, 1, At, B1); PG8_BAR; PG8_SCHED;
;             PG8_LDA(At, 0, 1); PG8_STAGE(PG8_SB(0, 0), b2, voffB); PG8_STAGE(PG8_SB(0, 1), b2 + hstep, voffB); PG8_STAGE(PG8_SA(0, 0), a2, voffA);
.LBB0_412:
	ds_read_b128 v[146:149], v152
	ds_read_b128 v[156:159], v152 offset:1024
	ds_read_b128 v[160:163], v152 offset:2048
	ds_read_b128 v[164:167], v152 offset:3072
	ds_read_b128 v[168:171], v153
	ds_read_b128 v[172:175], v153 offset:1024
	ds_read_b128 v[176:179], v153 offset:2048
	ds_read_b128 v[180:183], v153 offset:3072
	s_add_u32 s24, s22, 0xfff80080
	s_addc_u32 s25, s23, -1
	s_cmp_eq_u32 s60, 28
	s_cselect_b32 s27, s15, s25
	s_cselect_b32 s26, s48, s24
	s_cselect_b32 s25, s13, s57
	s_cselect_b32 s24, s49, s56
	v_lshl_add_u64 v[216:217], s[22:23], 0, v[138:139]
	s_add_i32 m0, s21, 0xc000
	ds_read_b128 v[184:187], v154
	ds_read_b128 v[188:191], v154 offset:1024
	ds_read_b128 v[192:195], v154 offset:2048
	ds_read_b128 v[196:199], v154 offset:3072
	ds_read_b128 v[200:203], v154 offset:4096
	ds_read_b128 v[204:207], v154 offset:5120
	ds_read_b128 v[208:211], v154 offset:6144
	ds_read_b128 v[212:215], v154 offset:7168
	global_load_lds_dwordx4 v[216:217], off
	v_lshl_add_u64 v[216:217], s[22:23], 0, v[140:141]
	s_add_i32 m0, s21, 0xe000
	s_nop 0
	global_load_lds_dwordx4 v[216:217], off
	s_waitcnt vmcnt(8)
	s_waitcnt lgkmcnt(0)
	s_setprio 1
	s_barrier
	s_waitcnt lgkmcnt(0)
	v_mfma_f32_16x16x32_bf16 v[126:129], v[146:149], v[184:187], v[126:129]
	v_mfma_f32_16x16x32_bf16 v[122:125], v[160:163], v[184:187], v[122:125]
	v_mfma_f32_16x16x32_bf16 v[118:121], v[146:149], v[192:195], v[118:121]
	v_mfma_f32_16x16x32_bf16 v[110:113], v[160:163], v[192:195], v[110:113]
	v_mfma_f32_16x16x32_bf16 v[102:105], v[146:149], v[200:203], v[102:105]
	v_mfma_f32_16x16x32_bf16 v[94:97], v[160:163], v[200:203], v[94:97]
	v_mfma_f32_16x16x32_bf16 v[86:89], v[146:149], v[208:211], v[86:89]
	v_mfma_f32_16x16x32_bf16 v[78:81], v[160:163], v[208:211], v[78:81]
	v_mfma_f32_16x16x32_bf16 v[126:129], v[156:159], v[188:191], v[126:129]
	v_mfma_f32_16x16x32_bf16 v[122:125], v[164:167], v[188:191], v[122:125]
	v_mfma_f32_16x16x32_bf16 v[118:121], v[156:159], v[196:199], v[118:121]
	v_mfma_f32_16x16x32_bf16 v[110:113], v[164:167], v[196:199], v[110:113]
	v_mfma_f32_16x16x32_bf16 v[102:105], v[156:159], v[204:207], v[102:105]
	v_mfma_f32_16x16x32_bf16 v[94:97], v[164:167], v[204:207], v[94:97]
	v_mfma_f32_16x16x32_bf16 v[86:89], v[156:159], v[212:215], v[86:89]
	v_mfma_f32_16x16x32_bf16 v[78:81], v[164:167], v[212:215], v[78:81]
	s_setprio 0
	s_setprio 1
	v_mfma_f32_16x16x32_bf16 v[114:117], v[168:171], v[184:187], v[114:117]
	v_mfma_f32_16x16x32_bf16 v[106:109], v[176:179], v[184:187], v[106:109]
	v_mfma_f32_16x16x32_bf16 v[98:101], v[168:171], v[192:195], v[98:101]
	v_mfma_f32_16x16x32_bf16 v[90:93], v[176:179], v[192:195], v[90:93]
	v_mfma_f32_16x16x32_bf16 v[82:85], v[168:171], v[200:203], v[82:85]
	v_mfma_f32_16x16x32_bf16 v[74:77], v[176:179], v[200:203], v[74:77]
	v_mfma_f32_16x16x32_bf16 v[70:73], v[168:171], v[208:211], v[70:73]
	v_mfma_f32_16x16x32_bf16 v[66:69], v[176:179], v[208:211], v[66:69]
	v_mfma_f32_16x16x32_bf16 v[114:117], v[172:175], v[188:191], v[114:117]
	v_mfma_f32_16x16x32_bf16 v[106:109], v[180:183], v[188:191], v[106:109]
	v_mfma_f32_16x16x32_bf16 v[98:101], v[172:175], v[196:199], v[98:101]
	v_mfma_f32_16x16x32_bf16 v[90:93], v[180:183], v[196:199], v[90:93]
	v_mfma_f32_16x16x32_bf16 v[82:85], v[172:175], v[204:207], v[82:85]
	v_mfma_f32_16x16x32_bf16 v[74:77], v[180:183], v[204:207], v[74:77]
	v_mfma_f32_16x16x32_bf16 v[70:73], v[172:175], v[212:215], v[70:73]
	v_mfma_f32_16x16x32_bf16 v[66:69], v[180:183], v[212:215], v[66:69]
	s_setprio 0
	s_barrier
	s_add_i32 s61, s44, s33
	v_lshl_add_u64 v[216:217], s[24:25], 0, v[134:135]
	s_mov_b32 m0, s61
	ds_read_b128 v[184:187], v154 offset:16384
	ds_read_b128 v[188:191], v154 offset:17408
	ds_read_b128 v[192:195], v154 offset:18432
	ds_read_b128 v[196:199], v154 offset:19456
	ds_read_b128 v[200:203], v154 offset:20480
	ds_read_b128 v[204:207], v154 offset:21504
	ds_read_b128 v[208:211], v154 offset:22528
	ds_read_b128 v[212:215], v154 offset:23552
	global_load_lds_dwordx4 v[216:217], off
	s_add_i32 m0, s61, 0x2000
	s_add_u32 s62, s24, 0x80000
	v_lshl_add_u64 v[218:219], s[24:25], 0, v[130:131]
	s_addc_u32 s63, s25, 0
	s_add_i32 s61, s45, s33
	global_load_lds_dwordx4 v[218:219], off
	v_lshl_add_u64 v[220:221], s[62:63], 0, v[134:135]
	s_mov_b32 m0, s61
	v_lshl_add_u64 v[222:223], s[26:27], 0, v[132:133]
	global_load_lds_dwordx4 v[220:221], off
	v_lshl_add_u64 v[220:221], s[62:63], 0, v[130:131]
	s_add_i32 m0, s61, 0x2000
	s_nop 0
	global_load_lds_dwordx4 v[220:221], off
	v_lshl_add_u64 v[220:221], s[26:27], 0, v[136:137]
	s_mov_b32 m0, s21
	s_nop 0
	global_load_lds_dwordx4 v[220:221], off
	s_mov_b32 m0, s36
	s_nop 0
	global_load_lds_dwordx4 v[222:223], off
	s_waitcnt vmcnt(8)
	s_waitcnt lgkmcnt(0)
	s_setprio 1
	s_barrier
; #define PG8_STAGE(bufoff, gbase, voff) do { _Pragma("unroll") for (int _i = 0; _i < 2; ++_i) \
;         __builtin_amdgcn_global_load_lds((const unsigned*)((const char*)(gbase) + (voff)[_i]), (PG8_LAS unsigned*)(lds + (bufoff) + ldsw + _i * 8192), 16, 0, 0); } while (0)
; #define PG8_LDA(dst, b, h) do { _Pragma("unroll") for (int m = 0; m < 4; ++m) _Pragma("unroll") for (int k = 0; k < 2; ++k) dst[m][k] = *(const PG8_LAS bf16x8*)(lds + PG8_SA(b, h) + aoff + m * 2048 + k * 1024); } while (0)
; #define PG8_LDB(dst, b, h) do { _Pragma("unroll") for (int n = 0; n < 2; ++n) _Pragma("unroll") for (int k = 0; k < 2; ++k) dst[n][k] = *(const PG8_LAS bf16x8*)(lds + PG8_SB(b, h) + boff + n * 2048 + k * 1024); } while (0)
; #define PG8_WAIT_V(n) asm volatile("s_waitcnt vmcnt(" #n ")" ::: "memory")
; #define PG8_WAIT_L(n) asm volatile("s_waitcnt lgkmcnt(" #n ")" ::: "memory")
; #define PG8_BAR __builtin_amdgcn_s_barrier()
; #define PG8_SCHED __builtin_amdgcn_sched_barrier(0)
; template <class Epi, class Sched, bool ALIGN_EPI = false, bool SP2 = false, bool FP8 = false>
; __device__ __forceinline__ void gemm_phase(PG8_LAS unsigned char* lds, const Gemm g, const Sched& S, const Epi& E) {
;     ...
;             PG8_WAIT_V(8); PG8_WAIT_L(0); PG8_BAR; PG8_MMA(0, 0, At, B0); PG8_MMA(0, 1, At, B1); PG8_BAR; PG8_SCHED;
;             PG8_LDA(At, 0, 1); PG8_STAGE(PG8_SB(0, 0), b2, voffB); PG8_STAGE(PG8_SB(0, 1), b2 + hstep, voffB); PG8_STAGE(PG8_SA(0, 0), a2, voffA);
;             PG8_WAIT_V(8); PG8_WAIT_L(0); PG8_BAR; PG8_MMA(1, 0, At, B0); PG8_MMA(1, 1, At, B1); PG8_BAR; PG8_SCHED;
;             PG8_LDB(B0, 1, 0); PG8_LDB(B1, 1, 1); PG8_SCHED; PG8_LDA(At, 1, 0); PG8_STAGE(PG8_SA(0, 1), a2 + hstep, voffA);
;             PG8_WAIT_V(8); PG8_WAIT_L(0); PG8_BAR; PG8_MMA(0, 0, At, B0); PG8_MMA(0, 1, At, B1); PG8_BAR; PG8_SCHED;
	s_waitcnt lgkmcnt(0)
	v_mfma_f32_16x16x32_bf16 v[62:65], v[146:149], v[184:187], v[62:65]
	v_mfma_f32_16x16x32_bf16 v[58:61], v[160:163], v[184:187], v[58:61]
	v_mfma_f32_16x16x32_bf16 v[54:57], v[146:149], v[192:195], v[54:57]
	v_mfma_f32_16x16x32_bf16 v[46:49], v[160:163], v[192:195], v[46:49]
	v_mfma_f32_16x16x32_bf16 v[38:41], v[146:149], v[200:203], v[38:41]
	v_mfma_f32_16x16x32_bf16 v[30:33], v[160:163], v[200:203], v[30:33]
	v_mfma_f32_16x16x32_bf16 v[22:25], v[146:149], v[208:211], v[22:25]
	v_mfma_f32_16x16x32_bf16 v[14:17], v[160:163], v[208:211], v[14:17]
	v_mfma_f32_16x16x32_bf16 v[62:65], v[156:159], v[188:191], v[62:65]
	v_mfma_f32_16x16x32_bf16 v[58:61], v[164:167], v[188:191], v[58:61]
	v_mfma_f32_16x16x32_bf16 v[54:57], v[156:159], v[196:199], v[54:57]
	v_mfma_f32_16x16x32_bf16 v[46:49], v[164:167], v[196:199], v[46:49]
	v_mfma_f32_16x16x32_bf16 v[38:41], v[156:159], v[204:207], v[38:41]
	v_mfma_f32_16x16x32_bf16 v[30:33], v[164:167], v[204:207], v[30:33]
	v_mfma_f32_16x16x32_bf16 v[22:25], v[156:159], v[212:215], v[22:25]
	v_mfma_f32_16x16x32_bf16 v[14:17], v[164:167], v[212:215], v[14:17]
	s_setprio 0
	s_setprio 1
	v_mfma_f32_16x16x32_bf16 v[50:53], v[168:171], v[184:187], v[50:53]
	v_mfma_f32_16x16x32_bf16 v[42:45], v[176:179], v[184:187], v[42:45]
	v_mfma_f32_16x16x32_bf16 v[34:37], v[168:171], v[192:195], v[34:37]
	v_mfma_f32_16x16x32_bf16 v[26:29], v[176:179], v[192:195], v[26:29]
	v_mfma_f32_16x16x32_bf16 v[18:21], v[168:171], v[200:203], v[18:21]
	v_mfma_f32_16x16x32_bf16 v[10:13], v[176:179], v[200:203], v[10:13]
	v_mfma_f32_16x16x32_bf16 v[6:9], v[168:171], v[208:211], v[6:9]
	v_mfma_f32_16x16x32_bf16 v[2:5], v[176:179], v[208:211], v[2:5]
	v_mfma_f32_16x16x32_bf16 v[50:53], v[172:175], v[188:191], v[50:53]
	v_mfma_f32_16x16x32_bf16 v[42:45], v[180:183], v[188:191], v[42:45]
	v_mfma_f32_16x16x32_bf16 v[34:37], v[172:175], v[196:199], v[34:37]
	v_mfma_f32_16x16x32_bf16 v[26:29], v[180:183], v[196:199], v[26:29]
	v_mfma_f32_16x16x32_bf16 v[18:21], v[172:175], v[204:207], v[18:21]
	v_mfma_f32_16x16x32_bf16 v[10:13], v[180:183], v[204:207], v[10:13]
	v_mfma_f32_16x16x32_bf16 v[6:9], v[172:175], v[212:215], v[6:9]
	v_mfma_f32_16x16x32_bf16 v[2:5], v[180:183], v[212:215], v[2:5]
	s_setprio 0
	s_barrier
	s_add_i32 s61, 0, 0x18000
	v_add_u32_e32 v155, s61, v150
	s_add_i32 s62, 0, 0x1c000
	ds_read_b128 v[146:149], v155
	ds_read_b128 v[156:159], v155 offset:1024
	ds_read_b128 v[160:163], v155 offset:2048
	ds_read_b128 v[164:167], v155 offset:3072
	v_add_u32_e32 v155, s62, v150
	ds_read_b128 v[168:171], v155
	ds_read_b128 v[172:175], v155 offset:1024
	ds_read_b128 v[176:179], v155 offset:2048
	ds_read_b128 v[180:183], v155 offset:3072
	s_add_u32 s26, s26, 0x80000
	s_addc_u32 s27, s27, 0
	s_mov_b32 m0, s37
	v_lshl_add_u64 v[224:225], s[26:27], 0, v[136:137]
	ds_read_b128 v[184:187], v154 offset:32768
	ds_read_b128 v[188:191], v154 offset:33792
	ds_read_b128 v[192:195], v154 offset:34816
	ds_read_b128 v[196:199], v154 offset:35840
	ds_read_b128 v[200:203], v154 offset:36864
	ds_read_b128 v[204:207], v154 offset:37888
	ds_read_b128 v[208:211], v154 offset:38912
	ds_read_b128 v[212:215], v154 offset:39936
	global_load_lds_dwordx4 v[224:225], off
	v_lshl_add_u64 v[224:225], s[26:27], 0, v[132:133]
	s_mov_b32 m0, s38
	s_nop 0
	global_load_lds_dwordx4 v[224:225], off
	s_waitcnt vmcnt(8)
	s_waitcnt lgkmcnt(0)
	s_setprio 1
	s_barrier
	s_waitcnt lgkmcnt(0)
	v_mfma_f32_16x16x32_bf16 v[126:129], v[146:149], v[184:187], v[126:129]
	v_mfma_f32_16x16x32_bf16 v[122:125], v[160:163], v[184:187], v[122:125]
	v_mfma_f32_16x16x32_bf16 v[118:121], v[146:149], v[192:195], v[118:121]
	v_mfma_f32_16x16x32_bf16 v[110:113], v[160:163], v[192:195], v[110:113]
	v_mfma_f32_16x16x32_bf16 v[102:105], v[146:149], v[200:203], v[102:105]
	v_mfma_f32_16x16x32_bf16 v[94:97], v[160:163], v[200:203], v[94:97]
	v_mfma_f32_16x16x32_bf16 v[86:89], v[146:149], v[208:211], v[86:89]
	v_mfma_f32_16x16x32_bf16 v[78:81], v[160:163], v[208:211], v[78:81]
	v_mfma_f32_16x16x32_bf16 v[126:129], v[156:159], v[188:191], v[126:129]
	v_mfma_f32_16x16x32_bf16 v[122:125], v[164:167], v[188:191], v[122:125]
	v_mfma_f32_16x16x32_bf16 v[118:121], v[156:159], v[196:199], v[118:121]
	v_mfma_f32_16x16x32_bf16 v[110:113], v[164:167], v[196:199], v[110:113]
	v_mfma_f32_16x16x32_bf16 v[102:105], v[156:159], v[204:207], v[102:105]
	v_mfma_f32_16x16x32_bf16 v[94:97], v[164:167], v[204:207], v[94:97]
	v_mfma_f32_16x16x32_bf16 v[86:89], v[156:159], v[212:215], v[86:89]
	v_mfma_f32_16x16x32_bf16 v[78:81], v[164:167], v[212:215], v[78:81]
	s_setprio 0
	s_setprio 1
	v_mfma_f32_16x16x32_bf16 v[114:117], v[168:171], v[184:187], v[114:117]
	v_mfma_f32_16x16x32_bf16 v[106:109], v[176:179], v[184:187], v[106:109]
	v_mfma_f32_16x16x32_bf16 v[98:101], v[168:171], v[192:195], v[98:101]
	v_mfma_f32_16x16x32_bf16 v[90:93], v[176:179], v[192:195], v[90:93]
	v_mfma_f32_16x16x32_bf16 v[82:85], v[168:171], v[200:203], v[82:85]
	v_mfma_f32_16x16x32_bf16 v[74:77], v[176:179], v[200:203], v[74:77]
	v_mfma_f32_16x16x32_bf16 v[70:73], v[168:171], v[208:211], v[70:73]
	v_mfma_f32_16x16x32_bf16 v[66:69], v[176:179], v[208:211], v[66:69]
	v_mfma_f32_16x16x32_bf16 v[114:117], v[172:175], v[188:191], v[114:117]
	v_mfma_f32_16x16x32_bf16 v[106:109], v[180:183], v[188:191], v[106:109]
	v_mfma_f32_16x16x32_bf16 v[98:101], v[172:175], v[196:199], v[98:101]
	v_mfma_f32_16x16x32_bf16 v[90:93], v[180:183], v[196:199], v[90:93]
	v_mfma_f32_16x16x32_bf16 v[82:85], v[172:175], v[204:207], v[82:85]
	v_mfma_f32_16x16x32_bf16 v[74:77], v[180:183], v[204:207], v[74:77]
	v_mfma_f32_16x16x32_bf16 v[70:73], v[172:175], v[212:215], v[70:73]
	v_mfma_f32_16x16x32_bf16 v[66:69], v[180:183], v[212:215], v[66:69]
	s_setprio 0
	s_barrier
; #define PG8_STAGE(bufoff, gbase, voff) do { _Pragma("unroll") for (int _i = 0; _i < 2; ++_i) \
;         __builtin_amdgcn_global_load_lds((const unsigned*)((const char*)(gbase) + (voff)[_i]), (PG8_LAS unsigned*)(lds + (bufoff) + ldsw + _i * 8192), 16, 0, 0); } while (0)
; #define PG8_LDA(dst, b, h) do { _Pragma("unroll") for (int m = 0; m < 4; ++m) _Pragma("unroll") for (int k = 0; k < 2; ++k) dst[m][k] = *(const PG8_LAS bf16x8*)(lds + PG8_SA(b, h) + aoff + m * 2048 + k * 1024); } while (0)
; #define PG8_WAIT_V(n) asm volatile("s_waitcnt vmcnt(" #n ")" ::: "memory")
; #define PG8_WAIT_L(n) asm volatile("s_waitcnt lgkmcnt(" #n ")" ::: "memory")
; #define PG8_BAR __builtin_amdgcn_s_barrier()
; #define PG8_SCHED __builtin_amdgcn_sched_barrier(0)
; template <class Epi, class Sched, bool ALIGN_EPI = false, bool SP2 = false, bool FP8 = false>
; __device__ __forceinline__ void gemm_phase(PG8_LAS unsigned char* lds, const Gemm g, const Sched& S, const Epi& E) {
;     ...
;         for (int t = 0; t < nt; t += 2) {
;     ...
;             PG8_WAIT_V(8); PG8_WAIT_L(0); PG8_BAR; PG8_MMA(0, 0, At, B0); PG8_MMA(0, 1, At, B1); PG8_BAR; PG8_SCHED;
;             PG8_LDA(At, 1, 1); PG8_STAGE(PG8_SB(1, 0), b3, voffB); PG8_STAGE(PG8_SB(1, 1), b3 + hstep, voffB); PG8_STAGE(PG8_SA(1, 0), a3, voffA);
;             PG8_WAIT_V(8); PG8_WAIT_L(0); PG8_BAR; PG8_MMA(1, 0, At, B0); PG8_MMA(1, 1, At, B1); PG8_BAR; PG8_SCHED;
	s_add_i32 s26, s61, s33
	v_lshl_add_u64 v[216:217], v[216:217], 0, s[8:9]
	s_mov_b32 m0, s26
	ds_read_b128 v[184:187], v154 offset:49152
	ds_read_b128 v[188:191], v154 offset:50176
	ds_read_b128 v[192:195], v154 offset:51200
	ds_read_b128 v[196:199], v154 offset:52224
	ds_read_b128 v[200:203], v154 offset:53248
	ds_read_b128 v[204:207], v154 offset:54272
	ds_read_b128 v[208:211], v154 offset:55296
	ds_read_b128 v[212:215], v154 offset:56320
	global_load_lds_dwordx4 v[216:217], off
	s_add_i32 m0, s26, 0x2000
	s_add_u32 s24, s24, 0x80080
	v_lshl_add_u64 v[216:217], v[218:219], 0, s[8:9]
	s_addc_u32 s25, s25, 0
	s_add_i32 s26, s62, s33
	global_load_lds_dwordx4 v[216:217], off
	v_lshl_add_u64 v[216:217], s[24:25], 0, v[134:135]
	s_mov_b32 m0, s26
	s_nop 0
	global_load_lds_dwordx4 v[216:217], off
	v_lshl_add_u64 v[216:217], s[24:25], 0, v[130:131]
	s_add_i32 m0, s26, 0x2000
	s_nop 0
	global_load_lds_dwordx4 v[216:217], off
	v_lshl_add_u64 v[216:217], v[220:221], 0, s[8:9]
	s_mov_b32 m0, s41
	s_nop 0
	global_load_lds_dwordx4 v[216:217], off
	v_lshl_add_u64 v[216:217], v[222:223], 0, s[8:9]
	s_mov_b32 m0, s42
	s_nop 0
	global_load_lds_dwordx4 v[216:217], off
	s_waitcnt vmcnt(8)
	s_waitcnt lgkmcnt(0)
	s_setprio 1
	s_barrier
	s_waitcnt lgkmcnt(0)
	v_mfma_f32_16x16x32_bf16 v[62:65], v[146:149], v[184:187], v[62:65]
	v_mfma_f32_16x16x32_bf16 v[58:61], v[160:163], v[184:187], v[58:61]
	v_mfma_f32_16x16x32_bf16 v[54:57], v[146:149], v[192:195], v[54:57]
	v_mfma_f32_16x16x32_bf16 v[46:49], v[160:163], v[192:195], v[46:49]
	v_mfma_f32_16x16x32_bf16 v[38:41], v[146:149], v[200:203], v[38:41]
	v_mfma_f32_16x16x32_bf16 v[30:33], v[160:163], v[200:203], v[30:33]
	v_mfma_f32_16x16x32_bf16 v[22:25], v[146:149], v[208:211], v[22:25]
	v_mfma_f32_16x16x32_bf16 v[14:17], v[160:163], v[208:211], v[14:17]
	v_mfma_f32_16x16x32_bf16 v[62:65], v[156:159], v[188:191], v[62:65]
	v_mfma_f32_16x16x32_bf16 v[58:61], v[164:167], v[188:191], v[58:61]
	v_mfma_f32_16x16x32_bf16 v[54:57], v[156:159], v[196:199], v[54:57]
	v_mfma_f32_16x16x32_bf16 v[46:49], v[164:167], v[196:199], v[46:49]
	v_mfma_f32_16x16x32_bf16 v[38:41], v[156:159], v[204:207], v[38:41]
	v_mfma_f32_16x16x32_bf16 v[30:33], v[164:167], v[204:207], v[30:33]
	v_mfma_f32_16x16x32_bf16 v[22:25], v[156:159], v[212:215], v[22:25]
	v_mfma_f32_16x16x32_bf16 v[14:17], v[164:167], v[212:215], v[14:17]
	s_setprio 0
	s_setprio 1
	v_mfma_f32_16x16x32_bf16 v[50:53], v[168:171], v[184:187], v[50:53]
	v_mfma_f32_16x16x32_bf16 v[42:45], v[176:179], v[184:187], v[42:45]
	v_mfma_f32_16x16x32_bf16 v[34:37], v[168:171], v[192:195], v[34:37]
	v_mfma_f32_16x16x32_bf16 v[26:29], v[176:179], v[192:195], v[26:29]
	v_mfma_f32_16x16x32_bf16 v[18:21], v[168:171], v[200:203], v[18:21]
	v_mfma_f32_16x16x32_bf16 v[10:13], v[176:179], v[200:203], v[10:13]
	v_mfma_f32_16x16x32_bf16 v[6:9], v[168:171], v[208:211], v[6:9]
	v_mfma_f32_16x16x32_bf16 v[2:5], v[176:179], v[208:211], v[2:5]
	v_mfma_f32_16x16x32_bf16 v[50:53], v[172:175], v[188:191], v[50:53]
	v_mfma_f32_16x16x32_bf16 v[42:45], v[180:183], v[188:191], v[42:45]
	v_mfma_f32_16x16x32_bf16 v[34:37], v[172:175], v[196:199], v[34:37]
	v_mfma_f32_16x16x32_bf16 v[26:29], v[180:183], v[196:199], v[26:29]
	v_mfma_f32_16x16x32_bf16 v[18:21], v[172:175], v[204:207], v[18:21]
	v_mfma_f32_16x16x32_bf16 v[10:13], v[180:183], v[204:207], v[10:13]
	v_mfma_f32_16x16x32_bf16 v[6:9], v[172:175], v[212:215], v[6:9]
	v_mfma_f32_16x16x32_bf16 v[2:5], v[180:183], v[212:215], v[2:5]
	s_setprio 0
	s_add_i32 s60, s60, 2
	s_add_u32 s22, s22, 0x100
	s_addc_u32 s23, s23, 0
	s_add_u32 s56, s56, 0x100
	s_addc_u32 s57, s57, 0
	s_cmp_gt_u32 s60, 29
	s_barrier
	s_cbranch_scc0 .LBB0_412
	s_and_b64 vcc, exec, s[10:11]
	s_cbranch_vccz .LBB0_415
	s_barrier

; #define PG8_STAGE(bufoff, gbase, voff) do { _Pragma("unroll") for (int _i = 0; _i < 2; ++_i) \
;         __builtin_amdgcn_global_load_lds((const unsigned*)((const char*)(gbase) + (voff)[_i]), (PG8_LAS unsigned*)(lds + (bufoff) + ldsw + _i * 8192), 16, 0, 0); } while (0)
; #define PG8_LDA(dst, b, h) do { _Pragma("unroll") for (int m = 0; m < 4; ++m) _Pragma("unroll") for (int k = 0; k < 2; ++k) dst[m][k] = *(const PG8_LAS bf16x8*)(lds + PG8_SA(b, h) + aoff + m * 2048 + k * 1024); } while (0)
; #define PG8_LDB(dst, b, h) do { _Pragma("unroll") for (int n = 0; n < 2; ++n) _Pragma("unroll") for (int k = 0; k < 2; ++k) dst[n][k] = *(const PG8_LAS bf16x8*)(lds + PG8_SB(b, h) + boff + n * 2048 + k * 1024); } while (0)
; #define PG8_WAIT_V(n) asm volatile("s_waitcnt vmcnt(" #n ")" ::: "memory")
; #define PG8_WAIT_L(n) asm volatile("s_waitcnt lgkmcnt(" #n ")" ::: "memory")
; #define PG8_BAR __builtin_amdgcn_s_barrier()
; #define PG8_SCHED __builtin_amdgcn_sched_barrier(0)
; template <class Epi, class Sched, bool ALIGN_EPI = false, bool SP2 = false, bool FP8 = false>
; __device__ __forceinline__ void gemm_phase(PG8_LAS unsigned char* lds, const Gemm g, const Sched& S, const Epi& E) {
;     ...
;             const bool last = (t == nt - 2);
;             const char* a1 = cA + (size_t)(t + 1) * kstep;
;             const char* a2 = last ? nA : cA + (size_t)(t + 2) * kstep; const char* b2 = last ? nB : cB + (size_t)(t + 2) * kstep;
;             const char* a3 = a2 + kstep; const char* b3 = b2 + kstep;
;             if (last && has_next) S.a_ready(nxt);
;             if constexpr (SP2) {
;             PG8_LDB(B0, 0, 0); PG8_LDB(B1, 0, 1); PG8_SCHED; PG8_LDA(At, 0, 0); PG8_STAGE(PG8_SA(1, 1), a1 + hstep, voffA);
;             PG8_WAIT_V(8); PG8_WAIT_L(0); PG8_BAR; PG8_MMA(0, 0, At, B0); PG8_MMA(0, 1, At, B1); PG8_BAR; PG8_SCHED;
;             PG8_LDA(At, 0, 1); PG8_STAGE(PG8_SB(0, 0), b2, voffB); PG8_STAGE(PG8_SB(0, 1), b2 + hstep, voffB); PG8_STAGE(PG8_SA(0, 0), a2, voffA);
.LBB0_1006:
	ds_read_b128 v[130:133], v194
	ds_read_b128 v[134:137], v194 offset:1024
	ds_read_b128 v[138:141], v194 offset:2048
	ds_read_b128 v[142:145], v194 offset:3072
	ds_read_b128 v[146:149], v195
	ds_read_b128 v[150:153], v195 offset:1024
	ds_read_b128 v[170:173], v195 offset:2048
	ds_read_b128 v[174:177], v195 offset:3072
	s_add_u32 s24, s22, 0xfff80080
	s_addc_u32 s25, s23, -1
	s_cmp_eq_u32 s61, 28
	s_cselect_b32 s27, s15, s25
	s_cselect_b32 s26, s49, s24
	s_cselect_b32 s25, s13, s60
	s_cselect_b32 s24, s56, s57
	v_lshl_add_u64 v[190:191], s[22:23], 0, v[162:163]
	s_add_i32 m0, s21, 0xc000
	ds_read_b128 v[178:181], v196
	ds_read_b128 v[182:185], v196 offset:1024
	ds_read_b128 v[186:189], v196 offset:2048
	ds_read_b128 v[198:201], v196 offset:3072
	ds_read_b128 v[202:205], v196 offset:4096
	ds_read_b128 v[206:209], v196 offset:5120
	ds_read_b128 v[210:213], v196 offset:6144
	ds_read_b128 v[214:217], v196 offset:7168
	global_load_lds_dwordx4 v[190:191], off
	v_lshl_add_u64 v[190:191], s[22:23], 0, v[164:165]
	s_add_i32 m0, s21, 0xe000
	s_nop 0
	global_load_lds_dwordx4 v[190:191], off
	s_waitcnt vmcnt(8)
	s_waitcnt lgkmcnt(0)
	s_setprio 1
	s_barrier
	s_waitcnt lgkmcnt(0)
	v_mfma_f32_16x16x32_bf16 v[126:129], v[130:133], v[178:181], v[126:129]
	v_mfma_f32_16x16x32_bf16 v[122:125], v[138:141], v[178:181], v[122:125]
	v_mfma_f32_16x16x32_bf16 v[110:113], v[130:133], v[186:189], v[110:113]
	v_mfma_f32_16x16x32_bf16 v[106:109], v[138:141], v[186:189], v[106:109]
	v_mfma_f32_16x16x32_bf16 v[94:97], v[130:133], v[202:205], v[94:97]
	v_mfma_f32_16x16x32_bf16 v[90:93], v[138:141], v[202:205], v[90:93]
	v_mfma_f32_16x16x32_bf16 v[78:81], v[130:133], v[210:213], v[78:81]
	v_mfma_f32_16x16x32_bf16 v[74:77], v[138:141], v[210:213], v[74:77]
	v_mfma_f32_16x16x32_bf16 v[126:129], v[134:137], v[182:185], v[126:129]
	v_mfma_f32_16x16x32_bf16 v[122:125], v[142:145], v[182:185], v[122:125]
	v_mfma_f32_16x16x32_bf16 v[110:113], v[134:137], v[198:201], v[110:113]
	v_mfma_f32_16x16x32_bf16 v[106:109], v[142:145], v[198:201], v[106:109]
	v_mfma_f32_16x16x32_bf16 v[94:97], v[134:137], v[206:209], v[94:97]
	v_mfma_f32_16x16x32_bf16 v[90:93], v[142:145], v[206:209], v[90:93]
	v_mfma_f32_16x16x32_bf16 v[78:81], v[134:137], v[214:217], v[78:81]
	v_mfma_f32_16x16x32_bf16 v[74:77], v[142:145], v[214:217], v[74:77]
	s_setprio 0
	s_setprio 1
	v_mfma_f32_16x16x32_bf16 v[118:121], v[146:149], v[178:181], v[118:121]
	v_mfma_f32_16x16x32_bf16 v[114:117], v[170:173], v[178:181], v[114:117]
	v_mfma_f32_16x16x32_bf16 v[102:105], v[146:149], v[186:189], v[102:105]
	v_mfma_f32_16x16x32_bf16 v[98:101], v[170:173], v[186:189], v[98:101]
	v_mfma_f32_16x16x32_bf16 v[86:89], v[146:149], v[202:205], v[86:89]
	v_mfma_f32_16x16x32_bf16 v[82:85], v[170:173], v[202:205], v[82:85]
	v_mfma_f32_16x16x32_bf16 v[70:73], v[146:149], v[210:213], v[70:73]
	v_mfma_f32_16x16x32_bf16 v[66:69], v[170:173], v[210:213], v[66:69]
	v_mfma_f32_16x16x32_bf16 v[118:121], v[150:153], v[182:185], v[118:121]
	v_mfma_f32_16x16x32_bf16 v[114:117], v[174:177], v[182:185], v[114:117]
	v_mfma_f32_16x16x32_bf16 v[102:105], v[150:153], v[198:201], v[102:105]
	v_mfma_f32_16x16x32_bf16 v[98:101], v[174:177], v[198:201], v[98:101]
	v_mfma_f32_16x16x32_bf16 v[86:89], v[150:153], v[206:209], v[86:89]
	v_mfma_f32_16x16x32_bf16 v[82:85], v[174:177], v[206:209], v[82:85]
	v_mfma_f32_16x16x32_bf16 v[70:73], v[150:153], v[214:217], v[70:73]
	v_mfma_f32_16x16x32_bf16 v[66:69], v[174:177], v[214:217], v[66:69]
	s_setprio 0
	s_barrier
	s_add_i32 s62, s44, s33
	v_lshl_add_u64 v[190:191], s[24:25], 0, v[156:157]
	s_mov_b32 m0, s62
	ds_read_b128 v[178:181], v196 offset:16384
	ds_read_b128 v[182:185], v196 offset:17408
	ds_read_b128 v[186:189], v196 offset:18432
	ds_read_b128 v[198:201], v196 offset:19456
	ds_read_b128 v[202:205], v196 offset:20480
	ds_read_b128 v[206:209], v196 offset:21504
	ds_read_b128 v[210:213], v196 offset:22528
	ds_read_b128 v[214:217], v196 offset:23552
	global_load_lds_dwordx4 v[190:191], off
	s_add_i32 m0, s62, 0x2000
	s_add_u32 s62, s24, 0x80000
	v_lshl_add_u64 v[218:219], s[24:25], 0, v[160:161]
	s_addc_u32 s63, s25, 0
	s_add_i32 s68, s45, s33
	global_load_lds_dwordx4 v[218:219], off
	v_lshl_add_u64 v[220:221], s[62:63], 0, v[156:157]
	s_mov_b32 m0, s68
	v_lshl_add_u64 v[222:223], s[26:27], 0, v[158:159]
	global_load_lds_dwordx4 v[220:221], off
	v_lshl_add_u64 v[220:221], s[62:63], 0, v[160:161]
	s_add_i32 m0, s68, 0x2000
	s_nop 0
	global_load_lds_dwordx4 v[220:221], off
	v_lshl_add_u64 v[220:221], s[26:27], 0, v[154:155]
	s_mov_b32 m0, s21
	s_nop 0
	global_load_lds_dwordx4 v[220:221], off
	s_mov_b32 m0, s34
	s_nop 0
	global_load_lds_dwordx4 v[222:223], off
	s_waitcnt vmcnt(8)
	s_waitcnt lgkmcnt(0)
	s_setprio 1
	s_barrier
; #define PG8_STAGE(bufoff, gbase, voff) do { _Pragma("unroll") for (int _i = 0; _i < 2; ++_i) \
;         __builtin_amdgcn_global_load_lds((const unsigned*)((const char*)(gbase) + (voff)[_i]), (PG8_LAS unsigned*)(lds + (bufoff) + ldsw + _i * 8192), 16, 0, 0); } while (0)
; #define PG8_LDA(dst, b, h) do { _Pragma("unroll") for (int m = 0; m < 4; ++m) _Pragma("unroll") for (int k = 0; k < 2; ++k) dst[m][k] = *(const PG8_LAS bf16x8*)(lds + PG8_SA(b, h) + aoff + m * 2048 + k * 1024); } while (0)
; #define PG8_LDB(dst, b, h) do { _Pragma("unroll") for (int n = 0; n < 2; ++n) _Pragma("unroll") for (int k = 0; k < 2; ++k) dst[n][k] = *(const PG8_LAS bf16x8*)(lds + PG8_SB(b, h) + boff + n * 2048 + k * 1024); } while (0)
; #define PG8_WAIT_V(n) asm volatile("s_waitcnt vmcnt(" #n ")" ::: "memory")
; #define PG8_WAIT_L(n) asm volatile("s_waitcnt lgkmcnt(" #n ")" ::: "memory")
; #define PG8_BAR __builtin_amdgcn_s_barrier()
; #define PG8_SCHED __builtin_amdgcn_sched_barrier(0)
; template <class Epi, class Sched, bool ALIGN_EPI = false, bool SP2 = false, bool FP8 = false>
; __device__ __forceinline__ void gemm_phase(PG8_LAS unsigned char* lds, const Gemm g, const Sched& S, const Epi& E) {
;     ...
;             PG8_WAIT_V(8); PG8_WAIT_L(0); PG8_BAR; PG8_MMA(1, 0, At, B0); PG8_MMA(1, 1, At, B1); PG8_BAR; PG8_SCHED;
;             PG8_LDB(B0, 1, 0); PG8_LDB(B1, 1, 1); PG8_SCHED; PG8_LDA(At, 1, 0); PG8_STAGE(PG8_SA(0, 1), a2 + hstep, voffA);
;             PG8_WAIT_V(8); PG8_WAIT_L(0); PG8_BAR; PG8_MMA(0, 0, At, B0); PG8_MMA(0, 1, At, B1); PG8_BAR; PG8_SCHED;
	s_waitcnt lgkmcnt(0)
	v_mfma_f32_16x16x32_bf16 v[62:65], v[130:133], v[178:181], v[62:65]
	v_mfma_f32_16x16x32_bf16 v[58:61], v[138:141], v[178:181], v[58:61]
	v_mfma_f32_16x16x32_bf16 v[46:49], v[130:133], v[186:189], v[46:49]
	v_mfma_f32_16x16x32_bf16 v[42:45], v[138:141], v[186:189], v[42:45]
	v_mfma_f32_16x16x32_bf16 v[30:33], v[130:133], v[202:205], v[30:33]
	v_mfma_f32_16x16x32_bf16 v[26:29], v[138:141], v[202:205], v[26:29]
	v_mfma_f32_16x16x32_bf16 v[14:17], v[130:133], v[210:213], v[14:17]
	v_mfma_f32_16x16x32_bf16 v[10:13], v[138:141], v[210:213], v[10:13]
	v_mfma_f32_16x16x32_bf16 v[62:65], v[134:137], v[182:185], v[62:65]
	v_mfma_f32_16x16x32_bf16 v[58:61], v[142:145], v[182:185], v[58:61]
	v_mfma_f32_16x16x32_bf16 v[46:49], v[134:137], v[198:201], v[46:49]
	v_mfma_f32_16x16x32_bf16 v[42:45], v[142:145], v[198:201], v[42:45]
	v_mfma_f32_16x16x32_bf16 v[30:33], v[134:137], v[206:209], v[30:33]
	v_mfma_f32_16x16x32_bf16 v[26:29], v[142:145], v[206:209], v[26:29]
	v_mfma_f32_16x16x32_bf16 v[14:17], v[134:137], v[214:217], v[14:17]
	v_mfma_f32_16x16x32_bf16 v[10:13], v[142:145], v[214:217], v[10:13]
	s_setprio 0
	s_setprio 1
	v_mfma_f32_16x16x32_bf16 v[54:57], v[146:149], v[178:181], v[54:57]
	v_mfma_f32_16x16x32_bf16 v[50:53], v[170:173], v[178:181], v[50:53]
	v_mfma_f32_16x16x32_bf16 v[38:41], v[146:149], v[186:189], v[38:41]
	v_mfma_f32_16x16x32_bf16 v[34:37], v[170:173], v[186:189], v[34:37]
	v_mfma_f32_16x16x32_bf16 v[22:25], v[146:149], v[202:205], v[22:25]
	v_mfma_f32_16x16x32_bf16 v[18:21], v[170:173], v[202:205], v[18:21]
	v_mfma_f32_16x16x32_bf16 v[6:9], v[146:149], v[210:213], v[6:9]
	v_mfma_f32_16x16x32_bf16 v[2:5], v[170:173], v[210:213], v[2:5]
	v_mfma_f32_16x16x32_bf16 v[54:57], v[150:153], v[182:185], v[54:57]
	v_mfma_f32_16x16x32_bf16 v[50:53], v[174:177], v[182:185], v[50:53]
	v_mfma_f32_16x16x32_bf16 v[38:41], v[150:153], v[198:201], v[38:41]
	v_mfma_f32_16x16x32_bf16 v[34:37], v[174:177], v[198:201], v[34:37]
	v_mfma_f32_16x16x32_bf16 v[22:25], v[150:153], v[206:209], v[22:25]
	v_mfma_f32_16x16x32_bf16 v[18:21], v[174:177], v[206:209], v[18:21]
	v_mfma_f32_16x16x32_bf16 v[6:9], v[150:153], v[214:217], v[6:9]
	v_mfma_f32_16x16x32_bf16 v[2:5], v[174:177], v[214:217], v[2:5]
	s_setprio 0
	s_barrier
	s_add_i32 s62, 0, 0x18000
	s_add_i32 s63, 0, 0x1c000
	v_add_u32_e32 v142, s62, v192
	v_add_u32_e32 v174, s63, v192
	ds_read_b128 v[130:133], v142
	ds_read_b128 v[134:137], v142 offset:1024
	ds_read_b128 v[138:141], v142 offset:2048
	ds_read_b128 v[142:145], v142 offset:3072
	ds_read_b128 v[146:149], v174
	ds_read_b128 v[150:153], v174 offset:1024
	ds_read_b128 v[170:173], v174 offset:2048
	ds_read_b128 v[174:177], v174 offset:3072
	s_add_u32 s26, s26, 0x80000
	s_addc_u32 s27, s27, 0
	s_mov_b32 m0, s35
	v_lshl_add_u64 v[224:225], s[26:27], 0, v[154:155]
	ds_read_b128 v[178:181], v196 offset:32768
	ds_read_b128 v[182:185], v196 offset:33792
	ds_read_b128 v[186:189], v196 offset:34816
	ds_read_b128 v[198:201], v196 offset:35840
	ds_read_b128 v[202:205], v196 offset:36864
	ds_read_b128 v[206:209], v196 offset:37888
	ds_read_b128 v[210:213], v196 offset:38912
	ds_read_b128 v[214:217], v196 offset:39936
	global_load_lds_dwordx4 v[224:225], off
	v_lshl_add_u64 v[224:225], s[26:27], 0, v[158:159]
	s_mov_b32 m0, s36
	s_nop 0
	global_load_lds_dwordx4 v[224:225], off
	s_waitcnt vmcnt(8)
	s_waitcnt lgkmcnt(0)
	s_setprio 1
	s_barrier
	s_waitcnt lgkmcnt(0)
	v_mfma_f32_16x16x32_bf16 v[126:129], v[130:133], v[178:181], v[126:129]
	v_mfma_f32_16x16x32_bf16 v[122:125], v[138:141], v[178:181], v[122:125]
	v_mfma_f32_16x16x32_bf16 v[110:113], v[130:133], v[186:189], v[110:113]
	v_mfma_f32_16x16x32_bf16 v[106:109], v[138:141], v[186:189], v[106:109]
	v_mfma_f32_16x16x32_bf16 v[94:97], v[130:133], v[202:205], v[94:97]
	v_mfma_f32_16x16x32_bf16 v[90:93], v[138:141], v[202:205], v[90:93]
	v_mfma_f32_16x16x32_bf16 v[78:81], v[130:133], v[210:213], v[78:81]
	v_mfma_f32_16x16x32_bf16 v[74:77], v[138:141], v[210:213], v[74:77]
	v_mfma_f32_16x16x32_bf16 v[126:129], v[134:137], v[182:185], v[126:129]
	v_mfma_f32_16x16x32_bf16 v[122:125], v[142:145], v[182:185], v[122:125]
	v_mfma_f32_16x16x32_bf16 v[110:113], v[134:137], v[198:201], v[110:113]
	v_mfma_f32_16x16x32_bf16 v[106:109], v[142:145], v[198:201], v[106:109]
	v_mfma_f32_16x16x32_bf16 v[94:97], v[134:137], v[206:209], v[94:97]
	v_mfma_f32_16x16x32_bf16 v[90:93], v[142:145], v[206:209], v[90:93]
	v_mfma_f32_16x16x32_bf16 v[78:81], v[134:137], v[214:217], v[78:81]
	v_mfma_f32_16x16x32_bf16 v[74:77], v[142:145], v[214:217], v[74:77]
	s_setprio 0
	s_setprio 1
	v_mfma_f32_16x16x32_bf16 v[118:121], v[146:149], v[178:181], v[118:121]
	v_mfma_f32_16x16x32_bf16 v[114:117], v[170:173], v[178:181], v[114:117]
	v_mfma_f32_16x16x32_bf16 v[102:105], v[146:149], v[186:189], v[102:105]
	v_mfma_f32_16x16x32_bf16 v[98:101], v[170:173], v[186:189], v[98:101]
	v_mfma_f32_16x16x32_bf16 v[86:89], v[146:149], v[202:205], v[86:89]
	v_mfma_f32_16x16x32_bf16 v[82:85], v[170:173], v[202:205], v[82:85]
	v_mfma_f32_16x16x32_bf16 v[70:73], v[146:149], v[210:213], v[70:73]
	v_mfma_f32_16x16x32_bf16 v[66:69], v[170:173], v[210:213], v[66:69]
	v_mfma_f32_16x16x32_bf16 v[118:121], v[150:153], v[182:185], v[118:121]
	v_mfma_f32_16x16x32_bf16 v[114:117], v[174:177], v[182:185], v[114:117]
	v_mfma_f32_16x16x32_bf16 v[102:105], v[150:153], v[198:201], v[102:105]
	v_mfma_f32_16x16x32_bf16 v[98:101], v[174:177], v[198:201], v[98:101]
	v_mfma_f32_16x16x32_bf16 v[86:89], v[150:153], v[206:209], v[86:89]
	v_mfma_f32_16x16x32_bf16 v[82:85], v[174:177], v[206:209], v[82:85]
	v_mfma_f32_16x16x32_bf16 v[70:73], v[150:153], v[214:217], v[70:73]
	v_mfma_f32_16x16x32_bf16 v[66:69], v[174:177], v[214:217], v[66:69]
	s_setprio 0
	s_barrier
; #define PG8_STAGE(bufoff, gbase, voff) do { _Pragma("unroll") for (int _i = 0; _i < 2; ++_i) \
;         __builtin_amdgcn_global_load_lds((const unsigned*)((const char*)(gbase) + (voff)[_i]), (PG8_LAS unsigned*)(lds + (bufoff) + ldsw + _i * 8192), 16, 0, 0); } while (0)
; #define PG8_LDA(dst, b, h) do { _Pragma("unroll") for (int m = 0; m < 4; ++m) _Pragma("unroll") for (int k = 0; k < 2; ++k) dst[m][k] = *(const PG8_LAS bf16x8*)(lds + PG8_SA(b, h) + aoff + m * 2048 + k * 1024); } while (0)
; #define PG8_WAIT_V(n) asm volatile("s_waitcnt vmcnt(" #n ")" ::: "memory")
; #define PG8_WAIT_L(n) asm volatile("s_waitcnt lgkmcnt(" #n ")" ::: "memory")
; #define PG8_BAR __builtin_amdgcn_s_barrier()
; #define PG8_SCHED __builtin_amdgcn_sched_barrier(0)
; template <class Epi, class Sched, bool ALIGN_EPI = false, bool SP2 = false, bool FP8 = false>
; __device__ __forceinline__ void gemm_phase(PG8_LAS unsigned char* lds, const Gemm g, const Sched& S, const Epi& E) {
;     ...
;             PG8_LDA(At, 1, 1); PG8_STAGE(PG8_SB(1, 0), b3, voffB); PG8_STAGE(PG8_SB(1, 1), b3 + hstep, voffB); PG8_STAGE(PG8_SA(1, 0), a3, voffA);
;             PG8_WAIT_V(8); PG8_WAIT_L(0); PG8_BAR; PG8_MMA(1, 0, At, B0); PG8_MMA(1, 1, At, B1); PG8_BAR; PG8_SCHED;
	s_add_i32 s26, s62, s33
	v_lshl_add_u64 v[190:191], v[190:191], 0, s[4:5]
	s_mov_b32 m0, s26
	ds_read_b128 v[178:181], v196 offset:49152
	ds_read_b128 v[182:185], v196 offset:50176
	ds_read_b128 v[186:189], v196 offset:51200
	ds_read_b128 v[198:201], v196 offset:52224
	ds_read_b128 v[202:205], v196 offset:53248
	ds_read_b128 v[206:209], v196 offset:54272
	ds_read_b128 v[210:213], v196 offset:55296
	ds_read_b128 v[214:217], v196 offset:56320
	global_load_lds_dwordx4 v[190:191], off
	s_add_i32 m0, s26, 0x2000
	s_add_u32 s24, s24, 0x80080
	v_lshl_add_u64 v[190:191], v[218:219], 0, s[4:5]
	s_addc_u32 s25, s25, 0
	s_add_i32 s26, s63, s33
	global_load_lds_dwordx4 v[190:191], off
	v_lshl_add_u64 v[190:191], s[24:25], 0, v[156:157]
	s_mov_b32 m0, s26
	s_nop 0
	global_load_lds_dwordx4 v[190:191], off
	v_lshl_add_u64 v[190:191], s[24:25], 0, v[160:161]
	s_add_i32 m0, s26, 0x2000
	s_nop 0
	global_load_lds_dwordx4 v[190:191], off
	v_lshl_add_u64 v[190:191], v[220:221], 0, s[4:5]
	s_mov_b32 m0, s41
	s_nop 0
	global_load_lds_dwordx4 v[190:191], off
	v_lshl_add_u64 v[190:191], v[222:223], 0, s[4:5]
	s_mov_b32 m0, s42
	s_nop 0
	global_load_lds_dwordx4 v[190:191], off
	s_waitcnt vmcnt(8)
	s_waitcnt lgkmcnt(0)
	s_setprio 1
	s_barrier
	s_waitcnt lgkmcnt(0)
	v_mfma_f32_16x16x32_bf16 v[62:65], v[130:133], v[178:181], v[62:65]
	v_mfma_f32_16x16x32_bf16 v[58:61], v[138:141], v[178:181], v[58:61]
	v_mfma_f32_16x16x32_bf16 v[46:49], v[130:133], v[186:189], v[46:49]
	v_mfma_f32_16x16x32_bf16 v[42:45], v[138:141], v[186:189], v[42:45]
	v_mfma_f32_16x16x32_bf16 v[30:33], v[130:133], v[202:205], v[30:33]
	v_mfma_f32_16x16x32_bf16 v[26:29], v[138:141], v[202:205], v[26:29]
	v_mfma_f32_16x16x32_bf16 v[14:17], v[130:133], v[210:213], v[14:17]
	v_mfma_f32_16x16x32_bf16 v[10:13], v[138:141], v[210:213], v[10:13]
	v_mfma_f32_16x16x32_bf16 v[62:65], v[134:137], v[182:185], v[62:65]
	v_mfma_f32_16x16x32_bf16 v[58:61], v[142:145], v[182:185], v[58:61]
	v_mfma_f32_16x16x32_bf16 v[46:49], v[134:137], v[198:201], v[46:49]
	v_mfma_f32_16x16x32_bf16 v[42:45], v[142:145], v[198:201], v[42:45]
	v_mfma_f32_16x16x32_bf16 v[30:33], v[134:137], v[206:209], v[30:33]
	v_mfma_f32_16x16x32_bf16 v[26:29], v[142:145], v[206:209], v[26:29]
	v_mfma_f32_16x16x32_bf16 v[14:17], v[134:137], v[214:217], v[14:17]
	v_mfma_f32_16x16x32_bf16 v[10:13], v[142:145], v[214:217], v[10:13]
	s_setprio 0
	s_setprio 1
	v_mfma_f32_16x16x32_bf16 v[54:57], v[146:149], v[178:181], v[54:57]
	v_mfma_f32_16x16x32_bf16 v[50:53], v[170:173], v[178:181], v[50:53]
	v_mfma_f32_16x16x32_bf16 v[38:41], v[146:149], v[186:189], v[38:41]
	v_mfma_f32_16x16x32_bf16 v[34:37], v[170:173], v[186:189], v[34:37]
	v_mfma_f32_16x16x32_bf16 v[22:25], v[146:149], v[202:205], v[22:25]
	v_mfma_f32_16x16x32_bf16 v[18:21], v[170:173], v[202:205], v[18:21]
	v_mfma_f32_16x16x32_bf16 v[6:9], v[146:149], v[210:213], v[6:9]
	v_mfma_f32_16x16x32_bf16 v[2:5], v[170:173], v[210:213], v[2:5]
	v_mfma_f32_16x16x32_bf16 v[54:57], v[150:153], v[182:185], v[54:57]
	v_mfma_f32_16x16x32_bf16 v[50:53], v[174:177], v[182:185], v[50:53]
	v_mfma_f32_16x16x32_bf16 v[38:41], v[150:153], v[198:201], v[38:41]
	v_mfma_f32_16x16x32_bf16 v[34:37], v[174:177], v[198:201], v[34:37]
	v_mfma_f32_16x16x32_bf16 v[22:25], v[150:153], v[206:209], v[22:25]
	v_mfma_f32_16x16x32_bf16 v[18:21], v[174:177], v[206:209], v[18:21]
	v_mfma_f32_16x16x32_bf16 v[6:9], v[150:153], v[214:217], v[6:9]
	v_mfma_f32_16x16x32_bf16 v[2:5], v[174:177], v[214:217], v[2:5]
	s_setprio 0
	s_add_i32 s61, s61, 2
	s_add_u32 s22, s22, 0x100
	s_addc_u32 s23, s23, 0
	s_add_u32 s57, s57, 0x100
	s_addc_u32 s60, s60, 0
	s_cmp_gt_u32 s61, 29
	s_barrier
	s_cbranch_scc0 .LBB0_1006
	s_and_b64 vcc, exec, s[8:9]
	s_cbranch_vccz .LBB0_1009
	s_barrier

; #define PG8_STAGE(bufoff, gbase, voff) do { _Pragma("unroll") for (int _i = 0; _i < 2; ++_i) \
;         __builtin_amdgcn_global_load_lds((const unsigned*)((const char*)(gbase) + (voff)[_i]), (PG8_LAS unsigned*)(lds + (bufoff) + ldsw + _i * 8192), 16, 0, 0); } while (0)
; #define PG8_LDA(dst, b, h) do { _Pragma("unroll") for (int m = 0; m < 4; ++m) _Pragma("unroll") for (int k = 0; k < 2; ++k) dst[m][k] = *(const PG8_LAS bf16x8*)(lds + PG8_SA(b, h) + aoff + m * 2048 + k * 1024); } while (0)
; #define PG8_LDB(dst, b, h) do { _Pragma("unroll") for (int n = 0; n < 2; ++n) _Pragma("unroll") for (int k = 0; k < 2; ++k) dst[n][k] = *(const PG8_LAS bf16x8*)(lds + PG8_SB(b, h) + boff + n * 2048 + k * 1024); } while (0)
; #define PG8_WAIT_V(n) asm volatile("s_waitcnt vmcnt(" #n ")" ::: "memory")
; #define PG8_WAIT_L(n) asm volatile("s_waitcnt lgkmcnt(" #n ")" ::: "memory")
; #define PG8_BAR __builtin_amdgcn_s_barrier()
; #define PG8_SCHED __builtin_amdgcn_sched_barrier(0)
; template <class Epi, class Sched, bool ALIGN_EPI = false, bool SP2 = false, bool FP8 = false>
; __device__ __forceinline__ void gemm_phase(PG8_LAS unsigned char* lds, const Gemm g, const Sched& S, const Epi& E) {
;     ...
;             const char* a1 = cA + (size_t)(t + 1) * kstep;
;             const char* a2 = last ? nA : cA + (size_t)(t + 2) * kstep; const char* b2 = last ? nB : cB + (size_t)(t + 2) * kstep;
;             const char* a3 = a2 + kstep; const char* b3 = b2 + kstep;
;             if (last && has_next) S.a_ready(nxt);
;             if constexpr (SP2) {
;             PG8_LDB(B0, 0, 0); PG8_LDB(B1, 0, 1); PG8_SCHED; PG8_LDA(At, 0, 0); PG8_STAGE(PG8_SA(1, 1), a1 + hstep, voffA);
;             PG8_WAIT_V(8); PG8_WAIT_L(0); PG8_BAR; PG8_MMA(0, 0, At, B0); PG8_MMA(0, 1, At, B1); PG8_BAR; PG8_SCHED;
;             PG8_LDA(At, 0, 1); PG8_STAGE(PG8_SB(0, 0), b2, voffB); PG8_STAGE(PG8_SB(0, 1), b2 + hstep, voffB); PG8_STAGE(PG8_SA(0, 0), a2, voffA);
;             PG8_WAIT_V(8); PG8_WAIT_L(0); PG8_BAR; PG8_MMA(1, 0, At, B0); PG8_MMA(1, 1, At, B1); PG8_BAR; PG8_SCHED;
.LBB0_1142:
	ds_read_b128 v[26:29], v188
	ds_read_b128 v[30:33], v188 offset:1024
	ds_read_b128 v[18:21], v188 offset:2048
	ds_read_b128 v[22:25], v188 offset:3072
	ds_read_b128 v[10:13], v189
	ds_read_b128 v[14:17], v189 offset:1024
	ds_read_b128 v[2:5], v189 offset:2048
	ds_read_b128 v[6:9], v189 offset:3072
	s_add_u32 s26, s24, 0xfffc0080
	s_addc_u32 s27, s25, -1
	s_cmp_eq_u32 s61, 12
	s_cselect_b32 s29, s17, s27
	s_cselect_b32 s28, s49, s26
	s_cselect_b32 s27, s15, s60
	s_cselect_b32 s26, s56, s57
	v_lshl_add_u64 v[216:217], s[24:25], 0, v[170:171]
	s_add_i32 m0, s23, 0xc000
	ds_read_b128 v[178:181], v190
	ds_read_b128 v[182:185], v190 offset:1024
	ds_read_b128 v[192:195], v190 offset:2048
	ds_read_b128 v[196:199], v190 offset:3072
	ds_read_b128 v[200:203], v190 offset:4096
	ds_read_b128 v[204:207], v190 offset:5120
	ds_read_b128 v[208:211], v190 offset:6144
	ds_read_b128 v[212:215], v190 offset:7168
	global_load_lds_dwordx4 v[216:217], off
	v_lshl_add_u64 v[216:217], s[24:25], 0, v[172:173]
	s_add_i32 m0, s23, 0xe000
	s_nop 0
	global_load_lds_dwordx4 v[216:217], off
	s_waitcnt vmcnt(8)
	s_waitcnt lgkmcnt(0)
	s_setprio 1
	s_barrier
	s_waitcnt lgkmcnt(0)
	v_mfma_f32_16x16x128_f8f6f4 v[158:161], v[26:33], v[178:185], v[158:161]
	v_mfma_f32_16x16x128_f8f6f4 v[150:153], v[18:25], v[178:185], v[150:153]
	v_mfma_f32_16x16x128_f8f6f4 v[142:145], v[26:33], v[192:199], v[142:145]
	v_mfma_f32_16x16x128_f8f6f4 v[134:137], v[18:25], v[192:199], v[134:137]
	v_mfma_f32_16x16x128_f8f6f4 v[126:129], v[26:33], v[200:207], v[126:129]
	v_mfma_f32_16x16x128_f8f6f4 v[118:121], v[18:25], v[200:207], v[118:121]
	v_mfma_f32_16x16x128_f8f6f4 v[110:113], v[26:33], v[208:215], v[110:113]
	v_mfma_f32_16x16x128_f8f6f4 v[102:105], v[18:25], v[208:215], v[102:105]
	s_setprio 0
	s_setprio 1
	v_mfma_f32_16x16x128_f8f6f4 v[154:157], v[10:17], v[178:185], v[154:157]
	v_mfma_f32_16x16x128_f8f6f4 v[146:149], v[2:9], v[178:185], v[146:149]
	v_mfma_f32_16x16x128_f8f6f4 v[138:141], v[10:17], v[192:199], v[138:141]
	v_mfma_f32_16x16x128_f8f6f4 v[130:133], v[2:9], v[192:199], v[130:133]
	v_mfma_f32_16x16x128_f8f6f4 v[122:125], v[10:17], v[200:207], v[122:125]
	v_mfma_f32_16x16x128_f8f6f4 v[114:117], v[2:9], v[200:207], v[114:117]
	v_mfma_f32_16x16x128_f8f6f4 v[106:109], v[10:17], v[208:215], v[106:109]
	v_mfma_f32_16x16x128_f8f6f4 v[98:101], v[2:9], v[208:215], v[98:101]
	s_setprio 0
	s_barrier
	s_add_i32 s62, s45, s34
	v_lshl_add_u64 v[178:179], s[26:27], 0, v[166:167]
	s_mov_b32 m0, s62
	ds_read_b128 v[192:195], v190 offset:16384
	ds_read_b128 v[196:199], v190 offset:17408
	ds_read_b128 v[200:203], v190 offset:18432
	ds_read_b128 v[204:207], v190 offset:19456
	ds_read_b128 v[208:211], v190 offset:20480
	ds_read_b128 v[212:215], v190 offset:21504
	ds_read_b128 v[216:219], v190 offset:22528
	ds_read_b128 v[220:223], v190 offset:23552
	global_load_lds_dwordx4 v[178:179], off
	s_add_i32 m0, s62, 0x2000
	s_add_u32 s62, s26, 0x40000
	v_lshl_add_u64 v[180:181], s[26:27], 0, v[162:163]
	s_addc_u32 s63, s27, 0
	s_add_i32 s68, s46, s34
	global_load_lds_dwordx4 v[180:181], off
	v_lshl_add_u64 v[182:183], s[62:63], 0, v[166:167]
	s_mov_b32 m0, s68
	v_lshl_add_u64 v[184:185], s[28:29], 0, v[164:165]
	global_load_lds_dwordx4 v[182:183], off
	v_lshl_add_u64 v[182:183], s[62:63], 0, v[162:163]
	s_add_i32 m0, s68, 0x2000
	s_nop 0
	global_load_lds_dwordx4 v[182:183], off
	v_lshl_add_u64 v[182:183], s[28:29], 0, v[168:169]
	s_mov_b32 m0, s23
	s_nop 0
	global_load_lds_dwordx4 v[182:183], off
	s_mov_b32 m0, s37
	s_nop 0
	global_load_lds_dwordx4 v[184:185], off
	s_waitcnt vmcnt(8)
	s_waitcnt lgkmcnt(0)
	s_setprio 1
	s_barrier
	s_waitcnt lgkmcnt(0)
	v_mfma_f32_16x16x128_f8f6f4 v[94:97], v[26:33], v[192:199], v[94:97]
	v_mfma_f32_16x16x128_f8f6f4 v[86:89], v[18:25], v[192:199], v[86:89]
	v_mfma_f32_16x16x128_f8f6f4 v[78:81], v[26:33], v[200:207], v[78:81]
	v_mfma_f32_16x16x128_f8f6f4 v[70:73], v[18:25], v[200:207], v[70:73]
	v_mfma_f32_16x16x128_f8f6f4 v[62:65], v[26:33], v[208:215], v[62:65]
	v_mfma_f32_16x16x128_f8f6f4 v[54:57], v[18:25], v[208:215], v[54:57]
	v_mfma_f32_16x16x128_f8f6f4 v[46:49], v[26:33], v[216:223], v[46:49]
	v_mfma_f32_16x16x128_f8f6f4 v[38:41], v[18:25], v[216:223], v[38:41]
	s_setprio 0
	s_setprio 1
	v_mfma_f32_16x16x128_f8f6f4 v[90:93], v[10:17], v[192:199], v[90:93]
	v_mfma_f32_16x16x128_f8f6f4 v[82:85], v[2:9], v[192:199], v[82:85]
	v_mfma_f32_16x16x128_f8f6f4 v[74:77], v[10:17], v[200:207], v[74:77]
	v_mfma_f32_16x16x128_f8f6f4 v[66:69], v[2:9], v[200:207], v[66:69]
	v_mfma_f32_16x16x128_f8f6f4 v[58:61], v[10:17], v[208:215], v[58:61]
	v_mfma_f32_16x16x128_f8f6f4 v[50:53], v[2:9], v[208:215], v[50:53]
	v_mfma_f32_16x16x128_f8f6f4 v[42:45], v[10:17], v[216:223], v[42:45]
	v_mfma_f32_16x16x128_f8f6f4 v[34:37], v[2:9], v[216:223], v[34:37]
	s_setprio 0
	s_barrier
; #define PG8_STAGE(bufoff, gbase, voff) do { _Pragma("unroll") for (int _i = 0; _i < 2; ++_i) \
;         __builtin_amdgcn_global_load_lds((const unsigned*)((const char*)(gbase) + (voff)[_i]), (PG8_LAS unsigned*)(lds + (bufoff) + ldsw + _i * 8192), 16, 0, 0); } while (0)
; #define PG8_LDA(dst, b, h) do { _Pragma("unroll") for (int m = 0; m < 4; ++m) _Pragma("unroll") for (int k = 0; k < 2; ++k) dst[m][k] = *(const PG8_LAS bf16x8*)(lds + PG8_SA(b, h) + aoff + m * 2048 + k * 1024); } while (0)
; #define PG8_LDB(dst, b, h) do { _Pragma("unroll") for (int n = 0; n < 2; ++n) _Pragma("unroll") for (int k = 0; k < 2; ++k) dst[n][k] = *(const PG8_LAS bf16x8*)(lds + PG8_SB(b, h) + boff + n * 2048 + k * 1024); } while (0)
; #define PG8_WAIT_V(n) asm volatile("s_waitcnt vmcnt(" #n ")" ::: "memory")
; #define PG8_WAIT_L(n) asm volatile("s_waitcnt lgkmcnt(" #n ")" ::: "memory")
; #define PG8_BAR __builtin_amdgcn_s_barrier()
; #define PG8_SCHED __builtin_amdgcn_sched_barrier(0)
; template <class Epi, class Sched, bool ALIGN_EPI = false, bool SP2 = false, bool FP8 = false>
; __device__ __forceinline__ void gemm_phase(PG8_LAS unsigned char* lds, const Gemm g, const Sched& S, const Epi& E) {
;     ...
;             PG8_LDB(B0, 1, 0); PG8_LDB(B1, 1, 1); PG8_SCHED; PG8_LDA(At, 1, 0); PG8_STAGE(PG8_SA(0, 1), a2 + hstep, voffA);
;             PG8_WAIT_V(8); PG8_WAIT_L(0); PG8_BAR; PG8_MMA(0, 0, At, B0); PG8_MMA(0, 1, At, B1); PG8_BAR; PG8_SCHED;
;             PG8_LDA(At, 1, 1); PG8_STAGE(PG8_SB(1, 0), b3, voffB); PG8_STAGE(PG8_SB(1, 1), b3 + hstep, voffB); PG8_STAGE(PG8_SA(1, 0), a3, voffA);
;             PG8_WAIT_V(8); PG8_WAIT_L(0); PG8_BAR; PG8_MMA(1, 0, At, B0); PG8_MMA(1, 1, At, B1); PG8_BAR; PG8_SCHED;
	s_add_i32 s62, 0, 0x18000
	s_add_i32 s63, 0, 0x1c000
	v_add_u32_e32 v14, s62, v186
	v_add_u32_e32 v30, s63, v186
	ds_read_b128 v[2:5], v14
	ds_read_b128 v[6:9], v14 offset:1024
	ds_read_b128 v[10:13], v14 offset:2048
	ds_read_b128 v[14:17], v14 offset:3072
	ds_read_b128 v[18:21], v30
	ds_read_b128 v[22:25], v30 offset:1024
	ds_read_b128 v[26:29], v30 offset:2048
	ds_read_b128 v[30:33], v30 offset:3072
	s_add_u32 s28, s28, 0x40000
	s_addc_u32 s29, s29, 0
	s_mov_b32 m0, s38
	v_lshl_add_u64 v[224:225], s[28:29], 0, v[168:169]
	ds_read_b128 v[192:195], v190 offset:32768
	ds_read_b128 v[196:199], v190 offset:33792
	ds_read_b128 v[200:203], v190 offset:34816
	ds_read_b128 v[204:207], v190 offset:35840
	ds_read_b128 v[208:211], v190 offset:36864
	ds_read_b128 v[212:215], v190 offset:37888
	ds_read_b128 v[216:219], v190 offset:38912
	ds_read_b128 v[220:223], v190 offset:39936
	global_load_lds_dwordx4 v[224:225], off
	v_lshl_add_u64 v[224:225], s[28:29], 0, v[164:165]
	s_mov_b32 m0, s39
	s_nop 0
	global_load_lds_dwordx4 v[224:225], off
	s_waitcnt vmcnt(8)
	s_waitcnt lgkmcnt(0)
	s_setprio 1
	s_barrier
	s_waitcnt lgkmcnt(0)
	v_mfma_f32_16x16x128_f8f6f4 v[158:161], v[2:9], v[192:199], v[158:161]
	v_mfma_f32_16x16x128_f8f6f4 v[150:153], v[10:17], v[192:199], v[150:153]
	v_mfma_f32_16x16x128_f8f6f4 v[142:145], v[2:9], v[200:207], v[142:145]
	v_mfma_f32_16x16x128_f8f6f4 v[134:137], v[10:17], v[200:207], v[134:137]
	v_mfma_f32_16x16x128_f8f6f4 v[126:129], v[2:9], v[208:215], v[126:129]
	v_mfma_f32_16x16x128_f8f6f4 v[118:121], v[10:17], v[208:215], v[118:121]
	v_mfma_f32_16x16x128_f8f6f4 v[110:113], v[2:9], v[216:223], v[110:113]
	v_mfma_f32_16x16x128_f8f6f4 v[102:105], v[10:17], v[216:223], v[102:105]
	s_setprio 0
	s_setprio 1
	v_mfma_f32_16x16x128_f8f6f4 v[154:157], v[18:25], v[192:199], v[154:157]
	v_mfma_f32_16x16x128_f8f6f4 v[146:149], v[26:33], v[192:199], v[146:149]
	v_mfma_f32_16x16x128_f8f6f4 v[138:141], v[18:25], v[200:207], v[138:141]
	v_mfma_f32_16x16x128_f8f6f4 v[130:133], v[26:33], v[200:207], v[130:133]
	v_mfma_f32_16x16x128_f8f6f4 v[122:125], v[18:25], v[208:215], v[122:125]
	v_mfma_f32_16x16x128_f8f6f4 v[114:117], v[26:33], v[208:215], v[114:117]
	v_mfma_f32_16x16x128_f8f6f4 v[106:109], v[18:25], v[216:223], v[106:109]
	v_mfma_f32_16x16x128_f8f6f4 v[98:101], v[26:33], v[216:223], v[98:101]
	s_setprio 0
	s_barrier
	s_add_i32 s28, s62, s34
	v_lshl_add_u64 v[178:179], v[178:179], 0, s[8:9]
	s_mov_b32 m0, s28
	ds_read_b128 v[192:195], v190 offset:49152
	ds_read_b128 v[196:199], v190 offset:50176
	ds_read_b128 v[200:203], v190 offset:51200
	ds_read_b128 v[204:207], v190 offset:52224
	ds_read_b128 v[208:211], v190 offset:53248
	ds_read_b128 v[212:215], v190 offset:54272
	ds_read_b128 v[216:219], v190 offset:55296
	ds_read_b128 v[220:223], v190 offset:56320
	global_load_lds_dwordx4 v[178:179], off
	s_add_i32 m0, s28, 0x2000
	s_add_u32 s26, s26, 0x40080
	v_lshl_add_u64 v[178:179], v[180:181], 0, s[8:9]
	s_addc_u32 s27, s27, 0
	s_add_i32 s28, s63, s34
	global_load_lds_dwordx4 v[178:179], off
	v_lshl_add_u64 v[178:179], s[26:27], 0, v[166:167]
	s_mov_b32 m0, s28
	s_nop 0
	global_load_lds_dwordx4 v[178:179], off
	v_lshl_add_u64 v[178:179], s[26:27], 0, v[162:163]
	s_add_i32 m0, s28, 0x2000
	s_nop 0
	global_load_lds_dwordx4 v[178:179], off
	v_lshl_add_u64 v[178:179], v[182:183], 0, s[8:9]
	s_mov_b32 m0, s42
	s_nop 0
	global_load_lds_dwordx4 v[178:179], off
	v_lshl_add_u64 v[178:179], v[184:185], 0, s[8:9]
	s_mov_b32 m0, s43
	s_nop 0
	global_load_lds_dwordx4 v[178:179], off
	s_waitcnt vmcnt(8)
	s_waitcnt lgkmcnt(0)
	s_setprio 1
	s_barrier
	s_waitcnt lgkmcnt(0)
	v_mfma_f32_16x16x128_f8f6f4 v[94:97], v[2:9], v[192:199], v[94:97]
	v_mfma_f32_16x16x128_f8f6f4 v[86:89], v[10:17], v[192:199], v[86:89]
	v_mfma_f32_16x16x128_f8f6f4 v[78:81], v[2:9], v[200:207], v[78:81]
	v_mfma_f32_16x16x128_f8f6f4 v[70:73], v[10:17], v[200:207], v[70:73]
	v_mfma_f32_16x16x128_f8f6f4 v[62:65], v[2:9], v[208:215], v[62:65]
	v_mfma_f32_16x16x128_f8f6f4 v[54:57], v[10:17], v[208:215], v[54:57]
	v_mfma_f32_16x16x128_f8f6f4 v[46:49], v[2:9], v[216:223], v[46:49]
	v_mfma_f32_16x16x128_f8f6f4 v[38:41], v[10:17], v[216:223], v[38:41]
	s_setprio 0
	s_setprio 1
	v_mfma_f32_16x16x128_f8f6f4 v[90:93], v[18:25], v[192:199], v[90:93]
	v_mfma_f32_16x16x128_f8f6f4 v[82:85], v[26:33], v[192:199], v[82:85]
	v_mfma_f32_16x16x128_f8f6f4 v[74:77], v[18:25], v[200:207], v[74:77]
	v_mfma_f32_16x16x128_f8f6f4 v[66:69], v[26:33], v[200:207], v[66:69]
	v_mfma_f32_16x16x128_f8f6f4 v[58:61], v[18:25], v[208:215], v[58:61]
	v_mfma_f32_16x16x128_f8f6f4 v[50:53], v[26:33], v[208:215], v[50:53]
	v_mfma_f32_16x16x128_f8f6f4 v[42:45], v[18:25], v[216:223], v[42:45]
	v_mfma_f32_16x16x128_f8f6f4 v[34:37], v[26:33], v[216:223], v[34:37]
	s_setprio 0
	s_add_i32 s61, s61, 2
	s_add_u32 s24, s24, 0x100
	s_addc_u32 s25, s25, 0
	s_add_u32 s57, s57, 0x100
	s_addc_u32 s60, s60, 0
	s_cmp_gt_u32 s61, 13
	s_barrier
	s_cbranch_scc0 .LBB0_1142
	s_nop 15
	s_nop 15
	s_nop 15
	s_nop 15
	s_and_b64 vcc, exec, s[10:11]
	s_cbranch_vccz .LBB0_1145
	s_barrier

; #define PG8_STAGE(bufoff, gbase, voff) do { _Pragma("unroll") for (int _i = 0; _i < 2; ++_i) \
;         __builtin_amdgcn_global_load_lds((const unsigned*)((const char*)(gbase) + (voff)[_i]), (PG8_LAS unsigned*)(lds + (bufoff) + ldsw + _i * 8192), 16, 0, 0); } while (0)
; #define PG8_LDA(dst, b, h) do { _Pragma("unroll") for (int m = 0; m < 4; ++m) _Pragma("unroll") for (int k = 0; k < 2; ++k) dst[m][k] = *(const PG8_LAS bf16x8*)(lds + PG8_SA(b, h) + aoff + m * 2048 + k * 1024); } while (0)
; #define PG8_LDB(dst, b, h) do { _Pragma("unroll") for (int n = 0; n < 2; ++n) _Pragma("unroll") for (int k = 0; k < 2; ++k) dst[n][k] = *(const PG8_LAS bf16x8*)(lds + PG8_SB(b, h) + boff + n * 2048 + k * 1024); } while (0)
; #define PG8_WAIT_V(n) asm volatile("s_waitcnt vmcnt(" #n ")" ::: "memory")
; #define PG8_WAIT_L(n) asm volatile("s_waitcnt lgkmcnt(" #n ")" ::: "memory")
; #define PG8_BAR __builtin_amdgcn_s_barrier()
; #define PG8_SCHED __builtin_amdgcn_sched_barrier(0)
; template <class Epi, class Sched, bool ALIGN_EPI = false, bool SP2 = false, bool FP8 = false>
; __device__ __forceinline__ void gemm_phase(PG8_LAS unsigned char* lds, const Gemm g, const Sched& S, const Epi& E) {
;     ...
;             const char* a1 = cA + (size_t)(t + 1) * kstep;
;             const char* a2 = last ? nA : cA + (size_t)(t + 2) * kstep; const char* b2 = last ? nB : cB + (size_t)(t + 2) * kstep;
;             const char* a3 = a2 + kstep; const char* b3 = b2 + kstep;
;             if (last && has_next) S.a_ready(nxt);
;             if constexpr (SP2) {
;             PG8_LDB(B0, 0, 0); PG8_LDB(B1, 0, 1); PG8_SCHED; PG8_LDA(At, 0, 0); PG8_STAGE(PG8_SA(1, 1), a1 + hstep, voffA);
;             PG8_WAIT_V(8); PG8_WAIT_L(0); PG8_BAR; PG8_MMA(0, 0, At, B0); PG8_MMA(0, 1, At, B1); PG8_BAR; PG8_SCHED;
;             PG8_LDA(At, 0, 1); PG8_STAGE(PG8_SB(0, 0), b2, voffB); PG8_STAGE(PG8_SB(0, 1), b2 + hstep, voffB); PG8_STAGE(PG8_SA(0, 0), a2, voffA);
;             PG8_WAIT_V(8); PG8_WAIT_L(0); PG8_BAR; PG8_MMA(1, 0, At, B0); PG8_MMA(1, 1, At, B1); PG8_BAR; PG8_SCHED;
.LBB0_1225:
	ds_read_b128 v[26:29], v190
	ds_read_b128 v[30:33], v190 offset:1024
	ds_read_b128 v[18:21], v190 offset:2048
	ds_read_b128 v[22:25], v190 offset:3072
	ds_read_b128 v[10:13], v191
	ds_read_b128 v[14:17], v191 offset:1024
	ds_read_b128 v[2:5], v191 offset:2048
	ds_read_b128 v[6:9], v191 offset:3072
	s_add_u32 s30, s28, 0xfff50080
	s_addc_u32 s31, s29, -1
	s_cmp_eq_u32 s72, 40
	s_cselect_b32 s35, s9, s31
	s_cselect_b32 s34, s8, s30
	s_cselect_b32 s31, s27, s71
	s_cselect_b32 s30, s26, s70
	v_lshl_add_u64 v[186:187], s[28:29], 0, v[170:171]
	s_add_i32 m0, s39, 0xc000
	ds_read_b128 v[178:181], v192
	ds_read_b128 v[182:185], v192 offset:1024
	ds_read_b128 v[194:197], v192 offset:2048
	ds_read_b128 v[198:201], v192 offset:3072
	ds_read_b128 v[202:205], v192 offset:4096
	ds_read_b128 v[206:209], v192 offset:5120
	ds_read_b128 v[210:213], v192 offset:6144
	ds_read_b128 v[214:217], v192 offset:7168
	global_load_lds_dwordx4 v[186:187], off
	v_lshl_add_u64 v[186:187], s[28:29], 0, v[172:173]
	s_add_i32 m0, s39, 0xe000
	s_nop 0
	global_load_lds_dwordx4 v[186:187], off
	s_waitcnt vmcnt(8)
	s_waitcnt lgkmcnt(0)
	s_setprio 1
	s_barrier
	s_waitcnt lgkmcnt(0)
	v_mfma_f32_16x16x128_f8f6f4 v[158:161], v[26:33], v[178:185], v[158:161]
	v_mfma_f32_16x16x128_f8f6f4 v[154:157], v[18:25], v[178:185], v[154:157]
	v_mfma_f32_16x16x128_f8f6f4 v[142:145], v[26:33], v[194:201], v[142:145]
	v_mfma_f32_16x16x128_f8f6f4 v[138:141], v[18:25], v[194:201], v[138:141]
	v_mfma_f32_16x16x128_f8f6f4 v[126:129], v[26:33], v[202:209], v[126:129]
	v_mfma_f32_16x16x128_f8f6f4 v[122:125], v[18:25], v[202:209], v[122:125]
	v_mfma_f32_16x16x128_f8f6f4 v[110:113], v[26:33], v[210:217], v[110:113]
	v_mfma_f32_16x16x128_f8f6f4 v[106:109], v[18:25], v[210:217], v[106:109]
	s_setprio 0
	s_setprio 1
	v_mfma_f32_16x16x128_f8f6f4 v[150:153], v[10:17], v[178:185], v[150:153]
	v_mfma_f32_16x16x128_f8f6f4 v[146:149], v[2:9], v[178:185], v[146:149]
	v_mfma_f32_16x16x128_f8f6f4 v[134:137], v[10:17], v[194:201], v[134:137]
	v_mfma_f32_16x16x128_f8f6f4 v[130:133], v[2:9], v[194:201], v[130:133]
	v_mfma_f32_16x16x128_f8f6f4 v[118:121], v[10:17], v[202:209], v[118:121]
	v_mfma_f32_16x16x128_f8f6f4 v[114:117], v[2:9], v[202:209], v[114:117]
	v_mfma_f32_16x16x128_f8f6f4 v[102:105], v[10:17], v[210:217], v[102:105]
	v_mfma_f32_16x16x128_f8f6f4 v[98:101], v[2:9], v[210:217], v[98:101]
	s_setprio 0
	s_barrier
	s_add_i32 s73, s56, s38
	v_lshl_add_u64 v[178:179], s[30:31], 0, v[164:165]
	s_mov_b32 m0, s73
	ds_read_b128 v[194:197], v192 offset:16384
	ds_read_b128 v[198:201], v192 offset:17408
	ds_read_b128 v[202:205], v192 offset:18432
	ds_read_b128 v[206:209], v192 offset:19456
	ds_read_b128 v[210:213], v192 offset:20480
	ds_read_b128 v[214:217], v192 offset:21504
	ds_read_b128 v[218:221], v192 offset:22528
	ds_read_b128 v[222:225], v192 offset:23552
	global_load_lds_dwordx4 v[178:179], off
	s_add_i32 m0, s73, 0x2000
	s_add_u32 s74, s30, 0xb0000
	v_lshl_add_u64 v[180:181], s[30:31], 0, v[168:169]
	s_addc_u32 s75, s31, 0
	s_add_i32 s73, s57, s38
	global_load_lds_dwordx4 v[180:181], off
	v_lshl_add_u64 v[182:183], s[74:75], 0, v[164:165]
	s_mov_b32 m0, s73
	v_lshl_add_u64 v[184:185], s[34:35], 0, v[166:167]
	global_load_lds_dwordx4 v[182:183], off
	v_lshl_add_u64 v[182:183], s[74:75], 0, v[168:169]
	s_add_i32 m0, s73, 0x2000
	s_nop 0
	global_load_lds_dwordx4 v[182:183], off
	v_lshl_add_u64 v[182:183], s[34:35], 0, v[162:163]
	s_mov_b32 m0, s39
	s_nop 0
	global_load_lds_dwordx4 v[182:183], off
	s_mov_b32 m0, s40
	s_nop 0
	global_load_lds_dwordx4 v[184:185], off
	s_waitcnt vmcnt(8)
	s_waitcnt lgkmcnt(0)
	s_setprio 1
	s_barrier
	s_waitcnt lgkmcnt(0)
	v_mfma_f32_16x16x128_f8f6f4 v[94:97], v[26:33], v[194:201], v[94:97]
	v_mfma_f32_16x16x128_f8f6f4 v[90:93], v[18:25], v[194:201], v[90:93]
	v_mfma_f32_16x16x128_f8f6f4 v[78:81], v[26:33], v[202:209], v[78:81]
	v_mfma_f32_16x16x128_f8f6f4 v[74:77], v[18:25], v[202:209], v[74:77]
	v_mfma_f32_16x16x128_f8f6f4 v[62:65], v[26:33], v[210:217], v[62:65]
	v_mfma_f32_16x16x128_f8f6f4 v[58:61], v[18:25], v[210:217], v[58:61]
	v_mfma_f32_16x16x128_f8f6f4 v[46:49], v[26:33], v[218:225], v[46:49]
	v_mfma_f32_16x16x128_f8f6f4 v[42:45], v[18:25], v[218:225], v[42:45]
	s_setprio 0
	s_setprio 1
	v_mfma_f32_16x16x128_f8f6f4 v[86:89], v[10:17], v[194:201], v[86:89]
	v_mfma_f32_16x16x128_f8f6f4 v[82:85], v[2:9], v[194:201], v[82:85]
	v_mfma_f32_16x16x128_f8f6f4 v[70:73], v[10:17], v[202:209], v[70:73]
	v_mfma_f32_16x16x128_f8f6f4 v[66:69], v[2:9], v[202:209], v[66:69]
	v_mfma_f32_16x16x128_f8f6f4 v[54:57], v[10:17], v[210:217], v[54:57]
	v_mfma_f32_16x16x128_f8f6f4 v[50:53], v[2:9], v[210:217], v[50:53]
	v_mfma_f32_16x16x128_f8f6f4 v[38:41], v[10:17], v[218:225], v[38:41]
	v_mfma_f32_16x16x128_f8f6f4 v[34:37], v[2:9], v[218:225], v[34:37]
	s_setprio 0
	s_barrier
; #define PG8_STAGE(bufoff, gbase, voff) do { _Pragma("unroll") for (int _i = 0; _i < 2; ++_i) \
;         __builtin_amdgcn_global_load_lds((const unsigned*)((const char*)(gbase) + (voff)[_i]), (PG8_LAS unsigned*)(lds + (bufoff) + ldsw + _i * 8192), 16, 0, 0); } while (0)
; #define PG8_LDA(dst, b, h) do { _Pragma("unroll") for (int m = 0; m < 4; ++m) _Pragma("unroll") for (int k = 0; k < 2; ++k) dst[m][k] = *(const PG8_LAS bf16x8*)(lds + PG8_SA(b, h) + aoff + m * 2048 + k * 1024); } while (0)
; #define PG8_LDB(dst, b, h) do { _Pragma("unroll") for (int n = 0; n < 2; ++n) _Pragma("unroll") for (int k = 0; k < 2; ++k) dst[n][k] = *(const PG8_LAS bf16x8*)(lds + PG8_SB(b, h) + boff + n * 2048 + k * 1024); } while (0)
; #define PG8_WAIT_V(n) asm volatile("s_waitcnt vmcnt(" #n ")" ::: "memory")
; #define PG8_WAIT_L(n) asm volatile("s_waitcnt lgkmcnt(" #n ")" ::: "memory")
; #define PG8_BAR __builtin_amdgcn_s_barrier()
; #define PG8_SCHED __builtin_amdgcn_sched_barrier(0)
; template <class Epi, class Sched, bool ALIGN_EPI = false, bool SP2 = false, bool FP8 = false>
; __device__ __forceinline__ void gemm_phase(PG8_LAS unsigned char* lds, const Gemm g, const Sched& S, const Epi& E) {
;     ...
;             PG8_LDB(B0, 1, 0); PG8_LDB(B1, 1, 1); PG8_SCHED; PG8_LDA(At, 1, 0); PG8_STAGE(PG8_SA(0, 1), a2 + hstep, voffA);
;             PG8_WAIT_V(8); PG8_WAIT_L(0); PG8_BAR; PG8_MMA(0, 0, At, B0); PG8_MMA(0, 1, At, B1); PG8_BAR; PG8_SCHED;
;             PG8_LDA(At, 1, 1); PG8_STAGE(PG8_SB(1, 0), b3, voffB); PG8_STAGE(PG8_SB(1, 1), b3 + hstep, voffB); PG8_STAGE(PG8_SA(1, 0), a3, voffA);
;             PG8_WAIT_V(8); PG8_WAIT_L(0); PG8_BAR; PG8_MMA(1, 0, At, B0); PG8_MMA(1, 1, At, B1); PG8_BAR; PG8_SCHED;
	s_add_i32 s73, 0, 0x18000
	s_add_i32 s74, 0, 0x1c000
	v_add_u32_e32 v14, s73, v188
	v_add_u32_e32 v30, s74, v188
	ds_read_b128 v[2:5], v14
	ds_read_b128 v[6:9], v14 offset:1024
	ds_read_b128 v[10:13], v14 offset:2048
	ds_read_b128 v[14:17], v14 offset:3072
	ds_read_b128 v[18:21], v30
	ds_read_b128 v[22:25], v30 offset:1024
	ds_read_b128 v[26:29], v30 offset:2048
	ds_read_b128 v[30:33], v30 offset:3072
	s_add_u32 s34, s34, 0xb0000
	s_addc_u32 s35, s35, 0
	s_mov_b32 m0, s41
	v_lshl_add_u64 v[186:187], s[34:35], 0, v[162:163]
	ds_read_b128 v[194:197], v192 offset:32768
	ds_read_b128 v[198:201], v192 offset:33792
	ds_read_b128 v[202:205], v192 offset:34816
	ds_read_b128 v[206:209], v192 offset:35840
	ds_read_b128 v[210:213], v192 offset:36864
	ds_read_b128 v[214:217], v192 offset:37888
	ds_read_b128 v[218:221], v192 offset:38912
	ds_read_b128 v[222:225], v192 offset:39936
	global_load_lds_dwordx4 v[186:187], off
	v_lshl_add_u64 v[186:187], s[34:35], 0, v[166:167]
	s_mov_b32 m0, s42
	s_nop 0
	global_load_lds_dwordx4 v[186:187], off
	s_waitcnt vmcnt(8)
	s_waitcnt lgkmcnt(0)
	s_setprio 1
	s_barrier
	s_waitcnt lgkmcnt(0)
	v_mfma_f32_16x16x128_f8f6f4 v[158:161], v[2:9], v[194:201], v[158:161]
	v_mfma_f32_16x16x128_f8f6f4 v[154:157], v[10:17], v[194:201], v[154:157]
	v_mfma_f32_16x16x128_f8f6f4 v[142:145], v[2:9], v[202:209], v[142:145]
	v_mfma_f32_16x16x128_f8f6f4 v[138:141], v[10:17], v[202:209], v[138:141]
	v_mfma_f32_16x16x128_f8f6f4 v[126:129], v[2:9], v[210:217], v[126:129]
	v_mfma_f32_16x16x128_f8f6f4 v[122:125], v[10:17], v[210:217], v[122:125]
	v_mfma_f32_16x16x128_f8f6f4 v[110:113], v[2:9], v[218:225], v[110:113]
	v_mfma_f32_16x16x128_f8f6f4 v[106:109], v[10:17], v[218:225], v[106:109]
	s_setprio 0
	s_setprio 1
	v_mfma_f32_16x16x128_f8f6f4 v[150:153], v[18:25], v[194:201], v[150:153]
	v_mfma_f32_16x16x128_f8f6f4 v[146:149], v[26:33], v[194:201], v[146:149]
	v_mfma_f32_16x16x128_f8f6f4 v[134:137], v[18:25], v[202:209], v[134:137]
	v_mfma_f32_16x16x128_f8f6f4 v[130:133], v[26:33], v[202:209], v[130:133]
	v_mfma_f32_16x16x128_f8f6f4 v[118:121], v[18:25], v[210:217], v[118:121]
	v_mfma_f32_16x16x128_f8f6f4 v[114:117], v[26:33], v[210:217], v[114:117]
	v_mfma_f32_16x16x128_f8f6f4 v[102:105], v[18:25], v[218:225], v[102:105]
	v_mfma_f32_16x16x128_f8f6f4 v[98:101], v[26:33], v[218:225], v[98:101]
	s_setprio 0
	s_barrier
	s_add_i32 s34, s73, s38
	v_lshl_add_u64 v[178:179], v[178:179], 0, s[12:13]
	s_mov_b32 m0, s34
	ds_read_b128 v[194:197], v192 offset:49152
	ds_read_b128 v[198:201], v192 offset:50176
	ds_read_b128 v[202:205], v192 offset:51200
	ds_read_b128 v[206:209], v192 offset:52224
	ds_read_b128 v[210:213], v192 offset:53248
	ds_read_b128 v[214:217], v192 offset:54272
	ds_read_b128 v[218:221], v192 offset:55296
	ds_read_b128 v[222:225], v192 offset:56320
	global_load_lds_dwordx4 v[178:179], off
	s_add_i32 m0, s34, 0x2000
	s_add_u32 s30, s30, 0xb0080
	v_lshl_add_u64 v[178:179], v[180:181], 0, s[12:13]
	s_addc_u32 s31, s31, 0
	s_add_i32 s34, s74, s38
	global_load_lds_dwordx4 v[178:179], off
	v_lshl_add_u64 v[178:179], s[30:31], 0, v[164:165]
	s_mov_b32 m0, s34
	s_nop 0
	global_load_lds_dwordx4 v[178:179], off
	v_lshl_add_u64 v[178:179], s[30:31], 0, v[168:169]
	s_add_i32 m0, s34, 0x2000
	s_nop 0
	global_load_lds_dwordx4 v[178:179], off
	v_lshl_add_u64 v[178:179], v[182:183], 0, s[12:13]
	s_mov_b32 m0, s47
	s_nop 0
	global_load_lds_dwordx4 v[178:179], off
	v_lshl_add_u64 v[178:179], v[184:185], 0, s[12:13]
	s_mov_b32 m0, s48
	s_nop 0
	global_load_lds_dwordx4 v[178:179], off
	s_waitcnt vmcnt(8)
	s_waitcnt lgkmcnt(0)
	s_setprio 1
	s_barrier
	s_waitcnt lgkmcnt(0)
	v_mfma_f32_16x16x128_f8f6f4 v[94:97], v[2:9], v[194:201], v[94:97]
	v_mfma_f32_16x16x128_f8f6f4 v[90:93], v[10:17], v[194:201], v[90:93]
	v_mfma_f32_16x16x128_f8f6f4 v[78:81], v[2:9], v[202:209], v[78:81]
	v_mfma_f32_16x16x128_f8f6f4 v[74:77], v[10:17], v[202:209], v[74:77]
	v_mfma_f32_16x16x128_f8f6f4 v[62:65], v[2:9], v[210:217], v[62:65]
	v_mfma_f32_16x16x128_f8f6f4 v[58:61], v[10:17], v[210:217], v[58:61]
	v_mfma_f32_16x16x128_f8f6f4 v[46:49], v[2:9], v[218:225], v[46:49]
	v_mfma_f32_16x16x128_f8f6f4 v[42:45], v[10:17], v[218:225], v[42:45]
	s_setprio 0
	s_setprio 1
	v_mfma_f32_16x16x128_f8f6f4 v[86:89], v[18:25], v[194:201], v[86:89]
	v_mfma_f32_16x16x128_f8f6f4 v[82:85], v[26:33], v[194:201], v[82:85]
	v_mfma_f32_16x16x128_f8f6f4 v[70:73], v[18:25], v[202:209], v[70:73]
	v_mfma_f32_16x16x128_f8f6f4 v[66:69], v[26:33], v[202:209], v[66:69]
	v_mfma_f32_16x16x128_f8f6f4 v[54:57], v[18:25], v[210:217], v[54:57]
	v_mfma_f32_16x16x128_f8f6f4 v[50:53], v[26:33], v[210:217], v[50:53]
	v_mfma_f32_16x16x128_f8f6f4 v[38:41], v[18:25], v[218:225], v[38:41]
	v_mfma_f32_16x16x128_f8f6f4 v[34:37], v[26:33], v[218:225], v[34:37]
	s_setprio 0
	s_add_i32 s72, s72, 2
	s_add_u32 s28, s28, 0x100
	s_addc_u32 s29, s29, 0
	s_add_u32 s70, s70, 0x100
	s_addc_u32 s71, s71, 0
	s_cmp_gt_u32 s72, 41
	s_barrier
	s_cbranch_scc0 .LBB0_1225
	s_nop 15
	s_nop 15
	s_nop 15
	s_nop 15
	s_and_b64 vcc, exec, s[14:15]
	s_cbranch_vccz .LBB0_1228
	s_barrier

; #define PG8_STAGE(bufoff, gbase, voff) do { _Pragma("unroll") for (int _i = 0; _i < 2; ++_i) \
;         __builtin_amdgcn_global_load_lds((const unsigned*)((const char*)(gbase) + (voff)[_i]), (PG8_LAS unsigned*)(lds + (bufoff) + ldsw + _i * 8192), 16, 0, 0); } while (0)
; #define PG8_LDA(dst, b, h) do { _Pragma("unroll") for (int m = 0; m < 4; ++m) _Pragma("unroll") for (int k = 0; k < 2; ++k) dst[m][k] = *(const PG8_LAS bf16x8*)(lds + PG8_SA(b, h) + aoff + m * 2048 + k * 1024); } while (0)
; #define PG8_LDB(dst, b, h) do { _Pragma("unroll") for (int n = 0; n < 2; ++n) _Pragma("unroll") for (int k = 0; k < 2; ++k) dst[n][k] = *(const PG8_LAS bf16x8*)(lds + PG8_SB(b, h) + boff + n * 2048 + k * 1024); } while (0)
; #define PG8_WAIT_V(n) asm volatile("s_waitcnt vmcnt(" #n ")" ::: "memory")
; #define PG8_WAIT_L(n) asm volatile("s_waitcnt lgkmcnt(" #n ")" ::: "memory")
; #define PG8_BAR __builtin_amdgcn_s_barrier()
; #define PG8_SCHED __builtin_amdgcn_sched_barrier(0)
; template <class Epi, class Sched, bool ALIGN_EPI = false, bool SP2 = false, bool FP8 = false>
; __device__ __forceinline__ void gemm_phase(PG8_LAS unsigned char* lds, const Gemm g, const Sched& S, const Epi& E) {
;     ...
;             const char* a1 = cA + (size_t)(t + 1) * kstep;
;             const char* a2 = last ? nA : cA + (size_t)(t + 2) * kstep; const char* b2 = last ? nB : cB + (size_t)(t + 2) * kstep;
;             const char* a3 = a2 + kstep; const char* b3 = b2 + kstep;
;             if (last && has_next) S.a_ready(nxt);
;             if constexpr (SP2) {
;             PG8_LDB(B0, 0, 0); PG8_LDB(B1, 0, 1); PG8_SCHED; PG8_LDA(At, 0, 0); PG8_STAGE(PG8_SA(1, 1), a1 + hstep, voffA);
;             PG8_WAIT_V(8); PG8_WAIT_L(0); PG8_BAR; PG8_MMA(0, 0, At, B0); PG8_MMA(0, 1, At, B1); PG8_BAR; PG8_SCHED;
;             PG8_LDA(At, 0, 1); PG8_STAGE(PG8_SB(0, 0), b2, voffB); PG8_STAGE(PG8_SB(0, 1), b2 + hstep, voffB); PG8_STAGE(PG8_SA(0, 0), a2, voffA);
;             PG8_WAIT_V(8); PG8_WAIT_L(0); PG8_BAR; PG8_MMA(1, 0, At, B0); PG8_MMA(1, 1, At, B1); PG8_BAR; PG8_SCHED;
.LBB0_1358:
	ds_read_b128 v[146:149], v152
	ds_read_b128 v[156:159], v152 offset:1024
	ds_read_b128 v[160:163], v152 offset:2048
	ds_read_b128 v[164:167], v152 offset:3072
	ds_read_b128 v[168:171], v153
	ds_read_b128 v[172:175], v153 offset:1024
	ds_read_b128 v[176:179], v153 offset:2048
	ds_read_b128 v[180:183], v153 offset:3072
	s_add_u32 s26, s24, 0xfff80080
	s_addc_u32 s27, s25, -1
	s_cmp_eq_u32 s62, 28
	s_cselect_b32 s29, s17, s27
	s_cselect_b32 s28, s56, s26
	s_cselect_b32 s27, s15, s61
	s_cselect_b32 s26, s57, s60
	v_lshl_add_u64 v[216:217], s[24:25], 0, v[138:139]
	s_add_i32 m0, s23, 0xc000
	ds_read_b128 v[184:187], v154
	ds_read_b128 v[188:191], v154 offset:1024
	ds_read_b128 v[192:195], v154 offset:2048
	ds_read_b128 v[196:199], v154 offset:3072
	ds_read_b128 v[200:203], v154 offset:4096
	ds_read_b128 v[204:207], v154 offset:5120
	ds_read_b128 v[208:211], v154 offset:6144
	ds_read_b128 v[212:215], v154 offset:7168
	global_load_lds_dwordx4 v[216:217], off
	v_lshl_add_u64 v[216:217], s[24:25], 0, v[140:141]
	s_add_i32 m0, s23, 0xe000
	s_nop 0
	global_load_lds_dwordx4 v[216:217], off
	s_waitcnt vmcnt(8)
	s_waitcnt lgkmcnt(0)
	s_setprio 1
	s_barrier
	s_waitcnt lgkmcnt(0)
	v_mfma_f32_16x16x32_bf16 v[126:129], v[146:149], v[184:187], v[126:129]
	v_mfma_f32_16x16x32_bf16 v[122:125], v[160:163], v[184:187], v[122:125]
	v_mfma_f32_16x16x32_bf16 v[118:121], v[146:149], v[192:195], v[118:121]
	v_mfma_f32_16x16x32_bf16 v[110:113], v[160:163], v[192:195], v[110:113]
	v_mfma_f32_16x16x32_bf16 v[102:105], v[146:149], v[200:203], v[102:105]
	v_mfma_f32_16x16x32_bf16 v[94:97], v[160:163], v[200:203], v[94:97]
	v_mfma_f32_16x16x32_bf16 v[86:89], v[146:149], v[208:211], v[86:89]
	v_mfma_f32_16x16x32_bf16 v[78:81], v[160:163], v[208:211], v[78:81]
	v_mfma_f32_16x16x32_bf16 v[126:129], v[156:159], v[188:191], v[126:129]
	v_mfma_f32_16x16x32_bf16 v[122:125], v[164:167], v[188:191], v[122:125]
	v_mfma_f32_16x16x32_bf16 v[118:121], v[156:159], v[196:199], v[118:121]
	v_mfma_f32_16x16x32_bf16 v[110:113], v[164:167], v[196:199], v[110:113]
	v_mfma_f32_16x16x32_bf16 v[102:105], v[156:159], v[204:207], v[102:105]
	v_mfma_f32_16x16x32_bf16 v[94:97], v[164:167], v[204:207], v[94:97]
	v_mfma_f32_16x16x32_bf16 v[86:89], v[156:159], v[212:215], v[86:89]
	v_mfma_f32_16x16x32_bf16 v[78:81], v[164:167], v[212:215], v[78:81]
	s_setprio 0
	s_setprio 1
	v_mfma_f32_16x16x32_bf16 v[114:117], v[168:171], v[184:187], v[114:117]
	v_mfma_f32_16x16x32_bf16 v[106:109], v[176:179], v[184:187], v[106:109]
	v_mfma_f32_16x16x32_bf16 v[98:101], v[168:171], v[192:195], v[98:101]
	v_mfma_f32_16x16x32_bf16 v[90:93], v[176:179], v[192:195], v[90:93]
	v_mfma_f32_16x16x32_bf16 v[82:85], v[168:171], v[200:203], v[82:85]
	v_mfma_f32_16x16x32_bf16 v[74:77], v[176:179], v[200:203], v[74:77]
	v_mfma_f32_16x16x32_bf16 v[70:73], v[168:171], v[208:211], v[70:73]
	v_mfma_f32_16x16x32_bf16 v[66:69], v[176:179], v[208:211], v[66:69]
	v_mfma_f32_16x16x32_bf16 v[114:117], v[172:175], v[188:191], v[114:117]
	v_mfma_f32_16x16x32_bf16 v[106:109], v[180:183], v[188:191], v[106:109]
	v_mfma_f32_16x16x32_bf16 v[98:101], v[172:175], v[196:199], v[98:101]
	v_mfma_f32_16x16x32_bf16 v[90:93], v[180:183], v[196:199], v[90:93]
	v_mfma_f32_16x16x32_bf16 v[82:85], v[172:175], v[204:207], v[82:85]
	v_mfma_f32_16x16x32_bf16 v[74:77], v[180:183], v[204:207], v[74:77]
	v_mfma_f32_16x16x32_bf16 v[70:73], v[172:175], v[212:215], v[70:73]
	v_mfma_f32_16x16x32_bf16 v[66:69], v[180:183], v[212:215], v[66:69]
	s_setprio 0
	s_barrier
	s_add_i32 s63, s46, s35
	v_lshl_add_u64 v[216:217], s[26:27], 0, v[134:135]
	s_mov_b32 m0, s63
	ds_read_b128 v[184:187], v154 offset:16384
	ds_read_b128 v[188:191], v154 offset:17408
	ds_read_b128 v[192:195], v154 offset:18432
	ds_read_b128 v[196:199], v154 offset:19456
	ds_read_b128 v[200:203], v154 offset:20480
	ds_read_b128 v[204:207], v154 offset:21504
	ds_read_b128 v[208:211], v154 offset:22528
	ds_read_b128 v[212:215], v154 offset:23552
	global_load_lds_dwordx4 v[216:217], off
	s_add_i32 m0, s63, 0x2000
	s_add_u32 s68, s26, 0x80000
	v_lshl_add_u64 v[218:219], s[26:27], 0, v[130:131]
	s_addc_u32 s69, s27, 0
	s_add_i32 s63, s47, s35
	global_load_lds_dwordx4 v[218:219], off
	v_lshl_add_u64 v[220:221], s[68:69], 0, v[134:135]
	s_mov_b32 m0, s63
	v_lshl_add_u64 v[222:223], s[28:29], 0, v[132:133]
	global_load_lds_dwordx4 v[220:221], off
	v_lshl_add_u64 v[220:221], s[68:69], 0, v[130:131]
	s_add_i32 m0, s63, 0x2000
	s_nop 0
	global_load_lds_dwordx4 v[220:221], off
	v_lshl_add_u64 v[220:221], s[28:29], 0, v[136:137]
	s_mov_b32 m0, s23
	s_nop 0
	global_load_lds_dwordx4 v[220:221], off
	s_mov_b32 m0, s38
	s_nop 0
	global_load_lds_dwordx4 v[222:223], off
	s_waitcnt vmcnt(8)
	s_waitcnt lgkmcnt(0)
	s_setprio 1
	s_barrier
; #define PG8_STAGE(bufoff, gbase, voff) do { _Pragma("unroll") for (int _i = 0; _i < 2; ++_i) \
;         __builtin_amdgcn_global_load_lds((const unsigned*)((const char*)(gbase) + (voff)[_i]), (PG8_LAS unsigned*)(lds + (bufoff) + ldsw + _i * 8192), 16, 0, 0); } while (0)
; #define PG8_LDA(dst, b, h) do { _Pragma("unroll") for (int m = 0; m < 4; ++m) _Pragma("unroll") for (int k = 0; k < 2; ++k) dst[m][k] = *(const PG8_LAS bf16x8*)(lds + PG8_SA(b, h) + aoff + m * 2048 + k * 1024); } while (0)
; #define PG8_LDB(dst, b, h) do { _Pragma("unroll") for (int n = 0; n < 2; ++n) _Pragma("unroll") for (int k = 0; k < 2; ++k) dst[n][k] = *(const PG8_LAS bf16x8*)(lds + PG8_SB(b, h) + boff + n * 2048 + k * 1024); } while (0)
; #define PG8_WAIT_V(n) asm volatile("s_waitcnt vmcnt(" #n ")" ::: "memory")
; #define PG8_WAIT_L(n) asm volatile("s_waitcnt lgkmcnt(" #n ")" ::: "memory")
; #define PG8_BAR __builtin_amdgcn_s_barrier()
; #define PG8_SCHED __builtin_amdgcn_sched_barrier(0)
; template <class Epi, class Sched, bool ALIGN_EPI = false, bool SP2 = false, bool FP8 = false>
; __device__ __forceinline__ void gemm_phase(PG8_LAS unsigned char* lds, const Gemm g, const Sched& S, const Epi& E) {
;     ...
;             PG8_WAIT_V(8); PG8_WAIT_L(0); PG8_BAR; PG8_MMA(1, 0, At, B0); PG8_MMA(1, 1, At, B1); PG8_BAR; PG8_SCHED;
;             PG8_LDB(B0, 1, 0); PG8_LDB(B1, 1, 1); PG8_SCHED; PG8_LDA(At, 1, 0); PG8_STAGE(PG8_SA(0, 1), a2 + hstep, voffA);
;             PG8_WAIT_V(8); PG8_WAIT_L(0); PG8_BAR; PG8_MMA(0, 0, At, B0); PG8_MMA(0, 1, At, B1); PG8_BAR; PG8_SCHED;
	s_waitcnt lgkmcnt(0)
	v_mfma_f32_16x16x32_bf16 v[62:65], v[146:149], v[184:187], v[62:65]
	v_mfma_f32_16x16x32_bf16 v[58:61], v[160:163], v[184:187], v[58:61]
	v_mfma_f32_16x16x32_bf16 v[54:57], v[146:149], v[192:195], v[54:57]
	v_mfma_f32_16x16x32_bf16 v[46:49], v[160:163], v[192:195], v[46:49]
	v_mfma_f32_16x16x32_bf16 v[38:41], v[146:149], v[200:203], v[38:41]
	v_mfma_f32_16x16x32_bf16 v[30:33], v[160:163], v[200:203], v[30:33]
	v_mfma_f32_16x16x32_bf16 v[22:25], v[146:149], v[208:211], v[22:25]
	v_mfma_f32_16x16x32_bf16 v[14:17], v[160:163], v[208:211], v[14:17]
	v_mfma_f32_16x16x32_bf16 v[62:65], v[156:159], v[188:191], v[62:65]
	v_mfma_f32_16x16x32_bf16 v[58:61], v[164:167], v[188:191], v[58:61]
	v_mfma_f32_16x16x32_bf16 v[54:57], v[156:159], v[196:199], v[54:57]
	v_mfma_f32_16x16x32_bf16 v[46:49], v[164:167], v[196:199], v[46:49]
	v_mfma_f32_16x16x32_bf16 v[38:41], v[156:159], v[204:207], v[38:41]
	v_mfma_f32_16x16x32_bf16 v[30:33], v[164:167], v[204:207], v[30:33]
	v_mfma_f32_16x16x32_bf16 v[22:25], v[156:159], v[212:215], v[22:25]
	v_mfma_f32_16x16x32_bf16 v[14:17], v[164:167], v[212:215], v[14:17]
	s_setprio 0
	s_setprio 1
	v_mfma_f32_16x16x32_bf16 v[50:53], v[168:171], v[184:187], v[50:53]
	v_mfma_f32_16x16x32_bf16 v[42:45], v[176:179], v[184:187], v[42:45]
	v_mfma_f32_16x16x32_bf16 v[34:37], v[168:171], v[192:195], v[34:37]
	v_mfma_f32_16x16x32_bf16 v[26:29], v[176:179], v[192:195], v[26:29]
	v_mfma_f32_16x16x32_bf16 v[18:21], v[168:171], v[200:203], v[18:21]
	v_mfma_f32_16x16x32_bf16 v[10:13], v[176:179], v[200:203], v[10:13]
	v_mfma_f32_16x16x32_bf16 v[6:9], v[168:171], v[208:211], v[6:9]
	v_mfma_f32_16x16x32_bf16 v[2:5], v[176:179], v[208:211], v[2:5]
	v_mfma_f32_16x16x32_bf16 v[50:53], v[172:175], v[188:191], v[50:53]
	v_mfma_f32_16x16x32_bf16 v[42:45], v[180:183], v[188:191], v[42:45]
	v_mfma_f32_16x16x32_bf16 v[34:37], v[172:175], v[196:199], v[34:37]
	v_mfma_f32_16x16x32_bf16 v[26:29], v[180:183], v[196:199], v[26:29]
	v_mfma_f32_16x16x32_bf16 v[18:21], v[172:175], v[204:207], v[18:21]
	v_mfma_f32_16x16x32_bf16 v[10:13], v[180:183], v[204:207], v[10:13]
	v_mfma_f32_16x16x32_bf16 v[6:9], v[172:175], v[212:215], v[6:9]
	v_mfma_f32_16x16x32_bf16 v[2:5], v[180:183], v[212:215], v[2:5]
	s_setprio 0
	s_barrier
	s_add_i32 s63, 0, 0x18000
	v_add_u32_e32 v155, s63, v150
	s_add_i32 s68, 0, 0x1c000
	ds_read_b128 v[146:149], v155
	ds_read_b128 v[156:159], v155 offset:1024
	ds_read_b128 v[160:163], v155 offset:2048
	ds_read_b128 v[164:167], v155 offset:3072
	v_add_u32_e32 v155, s68, v150
	ds_read_b128 v[168:171], v155
	ds_read_b128 v[172:175], v155 offset:1024
	ds_read_b128 v[176:179], v155 offset:2048
	ds_read_b128 v[180:183], v155 offset:3072
	s_add_u32 s28, s28, 0x80000
	s_addc_u32 s29, s29, 0
	s_mov_b32 m0, s39
	v_lshl_add_u64 v[224:225], s[28:29], 0, v[136:137]
	ds_read_b128 v[184:187], v154 offset:32768
	ds_read_b128 v[188:191], v154 offset:33792
	ds_read_b128 v[192:195], v154 offset:34816
	ds_read_b128 v[196:199], v154 offset:35840
	ds_read_b128 v[200:203], v154 offset:36864
	ds_read_b128 v[204:207], v154 offset:37888
	ds_read_b128 v[208:211], v154 offset:38912
	ds_read_b128 v[212:215], v154 offset:39936
	global_load_lds_dwordx4 v[224:225], off
	v_lshl_add_u64 v[224:225], s[28:29], 0, v[132:133]
	s_mov_b32 m0, s40
	s_nop 0
	global_load_lds_dwordx4 v[224:225], off
	s_waitcnt vmcnt(8)
	s_waitcnt lgkmcnt(0)
	s_setprio 1
	s_barrier
	s_waitcnt lgkmcnt(0)
	v_mfma_f32_16x16x32_bf16 v[126:129], v[146:149], v[184:187], v[126:129]
	v_mfma_f32_16x16x32_bf16 v[122:125], v[160:163], v[184:187], v[122:125]
	v_mfma_f32_16x16x32_bf16 v[118:121], v[146:149], v[192:195], v[118:121]
	v_mfma_f32_16x16x32_bf16 v[110:113], v[160:163], v[192:195], v[110:113]
	v_mfma_f32_16x16x32_bf16 v[102:105], v[146:149], v[200:203], v[102:105]
	v_mfma_f32_16x16x32_bf16 v[94:97], v[160:163], v[200:203], v[94:97]
	v_mfma_f32_16x16x32_bf16 v[86:89], v[146:149], v[208:211], v[86:89]
	v_mfma_f32_16x16x32_bf16 v[78:81], v[160:163], v[208:211], v[78:81]
	v_mfma_f32_16x16x32_bf16 v[126:129], v[156:159], v[188:191], v[126:129]
	v_mfma_f32_16x16x32_bf16 v[122:125], v[164:167], v[188:191], v[122:125]
	v_mfma_f32_16x16x32_bf16 v[118:121], v[156:159], v[196:199], v[118:121]
	v_mfma_f32_16x16x32_bf16 v[110:113], v[164:167], v[196:199], v[110:113]
	v_mfma_f32_16x16x32_bf16 v[102:105], v[156:159], v[204:207], v[102:105]
	v_mfma_f32_16x16x32_bf16 v[94:97], v[164:167], v[204:207], v[94:97]
	v_mfma_f32_16x16x32_bf16 v[86:89], v[156:159], v[212:215], v[86:89]
	v_mfma_f32_16x16x32_bf16 v[78:81], v[164:167], v[212:215], v[78:81]
	s_setprio 0
	s_setprio 1
	v_mfma_f32_16x16x32_bf16 v[114:117], v[168:171], v[184:187], v[114:117]
	v_mfma_f32_16x16x32_bf16 v[106:109], v[176:179], v[184:187], v[106:109]
	v_mfma_f32_16x16x32_bf16 v[98:101], v[168:171], v[192:195], v[98:101]
	v_mfma_f32_16x16x32_bf16 v[90:93], v[176:179], v[192:195], v[90:93]
	v_mfma_f32_16x16x32_bf16 v[82:85], v[168:171], v[200:203], v[82:85]
	v_mfma_f32_16x16x32_bf16 v[74:77], v[176:179], v[200:203], v[74:77]
	v_mfma_f32_16x16x32_bf16 v[70:73], v[168:171], v[208:211], v[70:73]
	v_mfma_f32_16x16x32_bf16 v[66:69], v[176:179], v[208:211], v[66:69]
	v_mfma_f32_16x16x32_bf16 v[114:117], v[172:175], v[188:191], v[114:117]
	v_mfma_f32_16x16x32_bf16 v[106:109], v[180:183], v[188:191], v[106:109]
	v_mfma_f32_16x16x32_bf16 v[98:101], v[172:175], v[196:199], v[98:101]
	v_mfma_f32_16x16x32_bf16 v[90:93], v[180:183], v[196:199], v[90:93]
	v_mfma_f32_16x16x32_bf16 v[82:85], v[172:175], v[204:207], v[82:85]
	v_mfma_f32_16x16x32_bf16 v[74:77], v[180:183], v[204:207], v[74:77]
	v_mfma_f32_16x16x32_bf16 v[70:73], v[172:175], v[212:215], v[70:73]
	v_mfma_f32_16x16x32_bf16 v[66:69], v[180:183], v[212:215], v[66:69]
	s_setprio 0
	s_barrier
; #define PG8_STAGE(bufoff, gbase, voff) do { _Pragma("unroll") for (int _i = 0; _i < 2; ++_i) \
;         __builtin_amdgcn_global_load_lds((const unsigned*)((const char*)(gbase) + (voff)[_i]), (PG8_LAS unsigned*)(lds + (bufoff) + ldsw + _i * 8192), 16, 0, 0); } while (0)
; #define PG8_LDA(dst, b, h) do { _Pragma("unroll") for (int m = 0; m < 4; ++m) _Pragma("unroll") for (int k = 0; k < 2; ++k) dst[m][k] = *(const PG8_LAS bf16x8*)(lds + PG8_SA(b, h) + aoff + m * 2048 + k * 1024); } while (0)
; #define PG8_WAIT_V(n) asm volatile("s_waitcnt vmcnt(" #n ")" ::: "memory")
; #define PG8_WAIT_L(n) asm volatile("s_waitcnt lgkmcnt(" #n ")" ::: "memory")
; #define PG8_BAR __builtin_amdgcn_s_barrier()
; #define PG8_SCHED __builtin_amdgcn_sched_barrier(0)
; template <class Epi, class Sched, bool ALIGN_EPI = false, bool SP2 = false, bool FP8 = false>
; __device__ __forceinline__ void gemm_phase(PG8_LAS unsigned char* lds, const Gemm g, const Sched& S, const Epi& E) {
;     ...
;             PG8_LDA(At, 1, 1); PG8_STAGE(PG8_SB(1, 0), b3, voffB); PG8_STAGE(PG8_SB(1, 1), b3 + hstep, voffB); PG8_STAGE(PG8_SA(1, 0), a3, voffA);
;             PG8_WAIT_V(8); PG8_WAIT_L(0); PG8_BAR; PG8_MMA(1, 0, At, B0); PG8_MMA(1, 1, At, B1); PG8_BAR; PG8_SCHED;
	s_add_i32 s28, s63, s35
	v_lshl_add_u64 v[216:217], v[216:217], 0, s[10:11]
	s_mov_b32 m0, s28
	ds_read_b128 v[184:187], v154 offset:49152
	ds_read_b128 v[188:191], v154 offset:50176
	ds_read_b128 v[192:195], v154 offset:51200
	ds_read_b128 v[196:199], v154 offset:52224
	ds_read_b128 v[200:203], v154 offset:53248
	ds_read_b128 v[204:207], v154 offset:54272
	ds_read_b128 v[208:211], v154 offset:55296
	ds_read_b128 v[212:215], v154 offset:56320
	global_load_lds_dwordx4 v[216:217], off
	s_add_i32 m0, s28, 0x2000
	s_add_u32 s26, s26, 0x80080
	v_lshl_add_u64 v[216:217], v[218:219], 0, s[10:11]
	s_addc_u32 s27, s27, 0
	s_add_i32 s28, s68, s35
	global_load_lds_dwordx4 v[216:217], off
	v_lshl_add_u64 v[216:217], s[26:27], 0, v[134:135]
	s_mov_b32 m0, s28
	s_nop 0
	global_load_lds_dwordx4 v[216:217], off
	v_lshl_add_u64 v[216:217], s[26:27], 0, v[130:131]
	s_add_i32 m0, s28, 0x2000
	s_nop 0
	global_load_lds_dwordx4 v[216:217], off
	v_lshl_add_u64 v[216:217], v[220:221], 0, s[10:11]
	s_mov_b32 m0, s43
	s_nop 0
	global_load_lds_dwordx4 v[216:217], off
	v_lshl_add_u64 v[216:217], v[222:223], 0, s[10:11]
	s_mov_b32 m0, s44
	s_nop 0
	global_load_lds_dwordx4 v[216:217], off
	s_waitcnt vmcnt(8)
	s_waitcnt lgkmcnt(0)
	s_setprio 1
	s_barrier
	s_waitcnt lgkmcnt(0)
	v_mfma_f32_16x16x32_bf16 v[62:65], v[146:149], v[184:187], v[62:65]
	v_mfma_f32_16x16x32_bf16 v[58:61], v[160:163], v[184:187], v[58:61]
	v_mfma_f32_16x16x32_bf16 v[54:57], v[146:149], v[192:195], v[54:57]
	v_mfma_f32_16x16x32_bf16 v[46:49], v[160:163], v[192:195], v[46:49]
	v_mfma_f32_16x16x32_bf16 v[38:41], v[146:149], v[200:203], v[38:41]
	v_mfma_f32_16x16x32_bf16 v[30:33], v[160:163], v[200:203], v[30:33]
	v_mfma_f32_16x16x32_bf16 v[22:25], v[146:149], v[208:211], v[22:25]
	v_mfma_f32_16x16x32_bf16 v[14:17], v[160:163], v[208:211], v[14:17]
	v_mfma_f32_16x16x32_bf16 v[62:65], v[156:159], v[188:191], v[62:65]
	v_mfma_f32_16x16x32_bf16 v[58:61], v[164:167], v[188:191], v[58:61]
	v_mfma_f32_16x16x32_bf16 v[54:57], v[156:159], v[196:199], v[54:57]
	v_mfma_f32_16x16x32_bf16 v[46:49], v[164:167], v[196:199], v[46:49]
	v_mfma_f32_16x16x32_bf16 v[38:41], v[156:159], v[204:207], v[38:41]
	v_mfma_f32_16x16x32_bf16 v[30:33], v[164:167], v[204:207], v[30:33]
	v_mfma_f32_16x16x32_bf16 v[22:25], v[156:159], v[212:215], v[22:25]
	v_mfma_f32_16x16x32_bf16 v[14:17], v[164:167], v[212:215], v[14:17]
	s_setprio 0
	s_setprio 1
	v_mfma_f32_16x16x32_bf16 v[50:53], v[168:171], v[184:187], v[50:53]
	v_mfma_f32_16x16x32_bf16 v[42:45], v[176:179], v[184:187], v[42:45]
	v_mfma_f32_16x16x32_bf16 v[34:37], v[168:171], v[192:195], v[34:37]
	v_mfma_f32_16x16x32_bf16 v[26:29], v[176:179], v[192:195], v[26:29]
	v_mfma_f32_16x16x32_bf16 v[18:21], v[168:171], v[200:203], v[18:21]
	v_mfma_f32_16x16x32_bf16 v[10:13], v[176:179], v[200:203], v[10:13]
	v_mfma_f32_16x16x32_bf16 v[6:9], v[168:171], v[208:211], v[6:9]
	v_mfma_f32_16x16x32_bf16 v[2:5], v[176:179], v[208:211], v[2:5]
	v_mfma_f32_16x16x32_bf16 v[50:53], v[172:175], v[188:191], v[50:53]
	v_mfma_f32_16x16x32_bf16 v[42:45], v[180:183], v[188:191], v[42:45]
	v_mfma_f32_16x16x32_bf16 v[34:37], v[172:175], v[196:199], v[34:37]
	v_mfma_f32_16x16x32_bf16 v[26:29], v[180:183], v[196:199], v[26:29]
	v_mfma_f32_16x16x32_bf16 v[18:21], v[172:175], v[204:207], v[18:21]
	v_mfma_f32_16x16x32_bf16 v[10:13], v[180:183], v[204:207], v[10:13]
	v_mfma_f32_16x16x32_bf16 v[6:9], v[172:175], v[212:215], v[6:9]
	v_mfma_f32_16x16x32_bf16 v[2:5], v[180:183], v[212:215], v[2:5]
	s_setprio 0
	s_add_i32 s62, s62, 2
	s_add_u32 s24, s24, 0x100
	s_addc_u32 s25, s25, 0
	s_add_u32 s60, s60, 0x100
	s_addc_u32 s61, s61, 0
	s_cmp_gt_u32 s62, 29
	s_barrier
	s_cbranch_scc0 .LBB0_1358
	s_and_b64 vcc, exec, s[12:13]
	s_cbranch_vccz .LBB0_1361
	s_barrier

; #define PG8_STAGE(bufoff, gbase, voff) do { _Pragma("unroll") for (int _i = 0; _i < 2; ++_i) \
;         __builtin_amdgcn_global_load_lds((const unsigned*)((const char*)(gbase) + (voff)[_i]), (PG8_LAS unsigned*)(lds + (bufoff) + ldsw + _i * 8192), 16, 0, 0); } while (0)
; #define PG8_LDA(dst, b, h) do { _Pragma("unroll") for (int m = 0; m < 4; ++m) _Pragma("unroll") for (int k = 0; k < 2; ++k) dst[m][k] = *(const PG8_LAS bf16x8*)(lds + PG8_SA(b, h) + aoff + m * 2048 + k * 1024); } while (0)
; #define PG8_LDB(dst, b, h) do { _Pragma("unroll") for (int n = 0; n < 2; ++n) _Pragma("unroll") for (int k = 0; k < 2; ++k) dst[n][k] = *(const PG8_LAS bf16x8*)(lds + PG8_SB(b, h) + boff + n * 2048 + k * 1024); } while (0)
; #define PG8_WAIT_V(n) asm volatile("s_waitcnt vmcnt(" #n ")" ::: "memory")
; #define PG8_WAIT_L(n) asm volatile("s_waitcnt lgkmcnt(" #n ")" ::: "memory")
; #define PG8_BAR __builtin_amdgcn_s_barrier()
; #define PG8_SCHED __builtin_amdgcn_sched_barrier(0)
; template <class Epi, class Sched, bool ALIGN_EPI = false, bool SP2 = false, bool FP8 = false>
; __device__ __forceinline__ void gemm_phase(PG8_LAS unsigned char* lds, const Gemm g, const Sched& S, const Epi& E) {
;     ...
;             const char* a1 = cA + (size_t)(t + 1) * kstep;
;             const char* a2 = last ? nA : cA + (size_t)(t + 2) * kstep; const char* b2 = last ? nB : cB + (size_t)(t + 2) * kstep;
;             const char* a3 = a2 + kstep; const char* b3 = b2 + kstep;
;             if (last && has_next) S.a_ready(nxt);
;             if constexpr (SP2) {
;             PG8_LDB(B0, 0, 0); PG8_LDB(B1, 0, 1); PG8_SCHED; PG8_LDA(At, 0, 0); PG8_STAGE(PG8_SA(1, 1), a1 + hstep, voffA);
;             PG8_WAIT_V(8); PG8_WAIT_L(0); PG8_BAR; PG8_MMA(0, 0, At, B0); PG8_MMA(0, 1, At, B1); PG8_BAR; PG8_SCHED;
;             PG8_LDA(At, 0, 1); PG8_STAGE(PG8_SB(0, 0), b2, voffB); PG8_STAGE(PG8_SB(0, 1), b2 + hstep, voffB); PG8_STAGE(PG8_SA(0, 0), a2, voffA);
;             PG8_WAIT_V(8); PG8_WAIT_L(0); PG8_BAR; PG8_MMA(1, 0, At, B0); PG8_MMA(1, 1, At, B1); PG8_BAR; PG8_SCHED;
.LBB0_1952:
	ds_read_b128 v[130:133], v190
	ds_read_b128 v[134:137], v190 offset:1024
	ds_read_b128 v[138:141], v190 offset:2048
	ds_read_b128 v[142:145], v190 offset:3072
	ds_read_b128 v[162:165], v191
	ds_read_b128 v[166:169], v191 offset:1024
	ds_read_b128 v[170:173], v191 offset:2048
	ds_read_b128 v[174:177], v191 offset:3072
	s_add_u32 s36, s34, 0xfff80080
	s_addc_u32 s37, s35, -1
	s_cmp_eq_u32 s69, 28
	s_cselect_b32 s39, s25, s37
	s_cselect_b32 s38, s61, s36
	s_cselect_b32 s37, s23, s68
	s_cselect_b32 s36, s62, s63
	v_lshl_add_u64 v[186:187], s[34:35], 0, v[154:155]
	s_add_i32 m0, s31, 0xc000
	ds_read_b128 v[178:181], v192
	ds_read_b128 v[182:185], v192 offset:1024
	ds_read_b128 v[194:197], v192 offset:2048
	ds_read_b128 v[198:201], v192 offset:3072
	ds_read_b128 v[202:205], v192 offset:4096
	ds_read_b128 v[206:209], v192 offset:5120
	ds_read_b128 v[210:213], v192 offset:6144
	ds_read_b128 v[214:217], v192 offset:7168
	global_load_lds_dwordx4 v[186:187], off
	v_lshl_add_u64 v[186:187], s[34:35], 0, v[156:157]
	s_add_i32 m0, s31, 0xe000
	s_nop 0
	global_load_lds_dwordx4 v[186:187], off
	s_waitcnt vmcnt(8)
	s_waitcnt lgkmcnt(0)
	s_setprio 1
	s_barrier
	s_waitcnt lgkmcnt(0)
	v_mfma_f32_16x16x32_bf16 v[126:129], v[130:133], v[178:181], v[126:129]
	v_mfma_f32_16x16x32_bf16 v[122:125], v[138:141], v[178:181], v[122:125]
	v_mfma_f32_16x16x32_bf16 v[110:113], v[130:133], v[194:197], v[110:113]
	v_mfma_f32_16x16x32_bf16 v[106:109], v[138:141], v[194:197], v[106:109]
	v_mfma_f32_16x16x32_bf16 v[94:97], v[130:133], v[202:205], v[94:97]
	v_mfma_f32_16x16x32_bf16 v[90:93], v[138:141], v[202:205], v[90:93]
	v_mfma_f32_16x16x32_bf16 v[78:81], v[130:133], v[210:213], v[78:81]
	v_mfma_f32_16x16x32_bf16 v[74:77], v[138:141], v[210:213], v[74:77]
	v_mfma_f32_16x16x32_bf16 v[126:129], v[134:137], v[182:185], v[126:129]
	v_mfma_f32_16x16x32_bf16 v[122:125], v[142:145], v[182:185], v[122:125]
	v_mfma_f32_16x16x32_bf16 v[110:113], v[134:137], v[198:201], v[110:113]
	v_mfma_f32_16x16x32_bf16 v[106:109], v[142:145], v[198:201], v[106:109]
	v_mfma_f32_16x16x32_bf16 v[94:97], v[134:137], v[206:209], v[94:97]
	v_mfma_f32_16x16x32_bf16 v[90:93], v[142:145], v[206:209], v[90:93]
	v_mfma_f32_16x16x32_bf16 v[78:81], v[134:137], v[214:217], v[78:81]
	v_mfma_f32_16x16x32_bf16 v[74:77], v[142:145], v[214:217], v[74:77]
	s_setprio 0
	s_setprio 1
	v_mfma_f32_16x16x32_bf16 v[118:121], v[162:165], v[178:181], v[118:121]
	v_mfma_f32_16x16x32_bf16 v[114:117], v[170:173], v[178:181], v[114:117]
	v_mfma_f32_16x16x32_bf16 v[102:105], v[162:165], v[194:197], v[102:105]
	v_mfma_f32_16x16x32_bf16 v[98:101], v[170:173], v[194:197], v[98:101]
	v_mfma_f32_16x16x32_bf16 v[86:89], v[162:165], v[202:205], v[86:89]
	v_mfma_f32_16x16x32_bf16 v[82:85], v[170:173], v[202:205], v[82:85]
	v_mfma_f32_16x16x32_bf16 v[70:73], v[162:165], v[210:213], v[70:73]
	v_mfma_f32_16x16x32_bf16 v[66:69], v[170:173], v[210:213], v[66:69]
	v_mfma_f32_16x16x32_bf16 v[118:121], v[166:169], v[182:185], v[118:121]
	v_mfma_f32_16x16x32_bf16 v[114:117], v[174:177], v[182:185], v[114:117]
	v_mfma_f32_16x16x32_bf16 v[102:105], v[166:169], v[198:201], v[102:105]
	v_mfma_f32_16x16x32_bf16 v[98:101], v[174:177], v[198:201], v[98:101]
	v_mfma_f32_16x16x32_bf16 v[86:89], v[166:169], v[206:209], v[86:89]
	v_mfma_f32_16x16x32_bf16 v[82:85], v[174:177], v[206:209], v[82:85]
	v_mfma_f32_16x16x32_bf16 v[70:73], v[166:169], v[214:217], v[70:73]
	v_mfma_f32_16x16x32_bf16 v[66:69], v[174:177], v[214:217], v[66:69]
	s_setprio 0
	s_barrier
	s_add_i32 s70, s54, s43
	v_lshl_add_u64 v[186:187], s[36:37], 0, v[148:149]
	s_mov_b32 m0, s70
	ds_read_b128 v[178:181], v192 offset:16384
	ds_read_b128 v[182:185], v192 offset:17408
	ds_read_b128 v[194:197], v192 offset:18432
	ds_read_b128 v[198:201], v192 offset:19456
	ds_read_b128 v[202:205], v192 offset:20480
	ds_read_b128 v[206:209], v192 offset:21504
	ds_read_b128 v[210:213], v192 offset:22528
	ds_read_b128 v[214:217], v192 offset:23552
	global_load_lds_dwordx4 v[186:187], off
	s_add_i32 m0, s70, 0x2000
	s_add_u32 s70, s36, 0x80000
	v_lshl_add_u64 v[218:219], s[36:37], 0, v[152:153]
	s_addc_u32 s71, s37, 0
	s_add_i32 s72, s55, s43
	global_load_lds_dwordx4 v[218:219], off
	v_lshl_add_u64 v[220:221], s[70:71], 0, v[148:149]
	s_mov_b32 m0, s72
	v_lshl_add_u64 v[222:223], s[38:39], 0, v[150:151]
	global_load_lds_dwordx4 v[220:221], off
	v_lshl_add_u64 v[220:221], s[70:71], 0, v[152:153]
	s_add_i32 m0, s72, 0x2000
	s_nop 0
	global_load_lds_dwordx4 v[220:221], off
	v_lshl_add_u64 v[220:221], s[38:39], 0, v[146:147]
	s_mov_b32 m0, s31
	s_nop 0
	global_load_lds_dwordx4 v[220:221], off
	s_mov_b32 m0, s44
	s_nop 0
	global_load_lds_dwordx4 v[222:223], off
	s_waitcnt vmcnt(8)
	s_waitcnt lgkmcnt(0)
	s_setprio 1
	s_barrier
; #define PG8_STAGE(bufoff, gbase, voff) do { _Pragma("unroll") for (int _i = 0; _i < 2; ++_i) \
;         __builtin_amdgcn_global_load_lds((const unsigned*)((const char*)(gbase) + (voff)[_i]), (PG8_LAS unsigned*)(lds + (bufoff) + ldsw + _i * 8192), 16, 0, 0); } while (0)
; #define PG8_LDA(dst, b, h) do { _Pragma("unroll") for (int m = 0; m < 4; ++m) _Pragma("unroll") for (int k = 0; k < 2; ++k) dst[m][k] = *(const PG8_LAS bf16x8*)(lds + PG8_SA(b, h) + aoff + m * 2048 + k * 1024); } while (0)
; #define PG8_LDB(dst, b, h) do { _Pragma("unroll") for (int n = 0; n < 2; ++n) _Pragma("unroll") for (int k = 0; k < 2; ++k) dst[n][k] = *(const PG8_LAS bf16x8*)(lds + PG8_SB(b, h) + boff + n * 2048 + k * 1024); } while (0)
; #define PG8_WAIT_V(n) asm volatile("s_waitcnt vmcnt(" #n ")" ::: "memory")
; #define PG8_WAIT_L(n) asm volatile("s_waitcnt lgkmcnt(" #n ")" ::: "memory")
; #define PG8_BAR __builtin_amdgcn_s_barrier()
; #define PG8_SCHED __builtin_amdgcn_sched_barrier(0)
; template <class Epi, class Sched, bool ALIGN_EPI = false, bool SP2 = false, bool FP8 = false>
; __device__ __forceinline__ void gemm_phase(PG8_LAS unsigned char* lds, const Gemm g, const Sched& S, const Epi& E) {
;     ...
;             PG8_WAIT_V(8); PG8_WAIT_L(0); PG8_BAR; PG8_MMA(1, 0, At, B0); PG8_MMA(1, 1, At, B1); PG8_BAR; PG8_SCHED;
;             PG8_LDB(B0, 1, 0); PG8_LDB(B1, 1, 1); PG8_SCHED; PG8_LDA(At, 1, 0); PG8_STAGE(PG8_SA(0, 1), a2 + hstep, voffA);
;             PG8_WAIT_V(8); PG8_WAIT_L(0); PG8_BAR; PG8_MMA(0, 0, At, B0); PG8_MMA(0, 1, At, B1); PG8_BAR; PG8_SCHED;
	s_waitcnt lgkmcnt(0)
	v_mfma_f32_16x16x32_bf16 v[62:65], v[130:133], v[178:181], v[62:65]
	v_mfma_f32_16x16x32_bf16 v[58:61], v[138:141], v[178:181], v[58:61]
	v_mfma_f32_16x16x32_bf16 v[46:49], v[130:133], v[194:197], v[46:49]
	v_mfma_f32_16x16x32_bf16 v[42:45], v[138:141], v[194:197], v[42:45]
	v_mfma_f32_16x16x32_bf16 v[30:33], v[130:133], v[202:205], v[30:33]
	v_mfma_f32_16x16x32_bf16 v[26:29], v[138:141], v[202:205], v[26:29]
	v_mfma_f32_16x16x32_bf16 v[14:17], v[130:133], v[210:213], v[14:17]
	v_mfma_f32_16x16x32_bf16 v[10:13], v[138:141], v[210:213], v[10:13]
	v_mfma_f32_16x16x32_bf16 v[62:65], v[134:137], v[182:185], v[62:65]
	v_mfma_f32_16x16x32_bf16 v[58:61], v[142:145], v[182:185], v[58:61]
	v_mfma_f32_16x16x32_bf16 v[46:49], v[134:137], v[198:201], v[46:49]
	v_mfma_f32_16x16x32_bf16 v[42:45], v[142:145], v[198:201], v[42:45]
	v_mfma_f32_16x16x32_bf16 v[30:33], v[134:137], v[206:209], v[30:33]
	v_mfma_f32_16x16x32_bf16 v[26:29], v[142:145], v[206:209], v[26:29]
	v_mfma_f32_16x16x32_bf16 v[14:17], v[134:137], v[214:217], v[14:17]
	v_mfma_f32_16x16x32_bf16 v[10:13], v[142:145], v[214:217], v[10:13]
	s_setprio 0
	s_setprio 1
	v_mfma_f32_16x16x32_bf16 v[54:57], v[162:165], v[178:181], v[54:57]
	v_mfma_f32_16x16x32_bf16 v[50:53], v[170:173], v[178:181], v[50:53]
	v_mfma_f32_16x16x32_bf16 v[38:41], v[162:165], v[194:197], v[38:41]
	v_mfma_f32_16x16x32_bf16 v[34:37], v[170:173], v[194:197], v[34:37]
	v_mfma_f32_16x16x32_bf16 v[22:25], v[162:165], v[202:205], v[22:25]
	v_mfma_f32_16x16x32_bf16 v[18:21], v[170:173], v[202:205], v[18:21]
	v_mfma_f32_16x16x32_bf16 v[6:9], v[162:165], v[210:213], v[6:9]
	v_mfma_f32_16x16x32_bf16 v[2:5], v[170:173], v[210:213], v[2:5]
	v_mfma_f32_16x16x32_bf16 v[54:57], v[166:169], v[182:185], v[54:57]
	v_mfma_f32_16x16x32_bf16 v[50:53], v[174:177], v[182:185], v[50:53]
	v_mfma_f32_16x16x32_bf16 v[38:41], v[166:169], v[198:201], v[38:41]
	v_mfma_f32_16x16x32_bf16 v[34:37], v[174:177], v[198:201], v[34:37]
	v_mfma_f32_16x16x32_bf16 v[22:25], v[166:169], v[206:209], v[22:25]
	v_mfma_f32_16x16x32_bf16 v[18:21], v[174:177], v[206:209], v[18:21]
	v_mfma_f32_16x16x32_bf16 v[6:9], v[166:169], v[214:217], v[6:9]
	v_mfma_f32_16x16x32_bf16 v[2:5], v[174:177], v[214:217], v[2:5]
	s_setprio 0
	s_barrier
	s_add_i32 s70, 0, 0x18000
	s_add_i32 s71, 0, 0x1c000
	v_add_u32_e32 v142, s70, v188
	v_add_u32_e32 v174, s71, v188
	ds_read_b128 v[130:133], v142
	ds_read_b128 v[134:137], v142 offset:1024
	ds_read_b128 v[138:141], v142 offset:2048
	ds_read_b128 v[142:145], v142 offset:3072
	ds_read_b128 v[162:165], v174
	ds_read_b128 v[166:169], v174 offset:1024
	ds_read_b128 v[170:173], v174 offset:2048
	ds_read_b128 v[174:177], v174 offset:3072
	s_add_u32 s38, s38, 0x80000
	s_addc_u32 s39, s39, 0
	s_mov_b32 m0, s45
	v_lshl_add_u64 v[224:225], s[38:39], 0, v[146:147]
	ds_read_b128 v[178:181], v192 offset:32768
	ds_read_b128 v[182:185], v192 offset:33792
	ds_read_b128 v[194:197], v192 offset:34816
	ds_read_b128 v[198:201], v192 offset:35840
	ds_read_b128 v[202:205], v192 offset:36864
	ds_read_b128 v[206:209], v192 offset:37888
	ds_read_b128 v[210:213], v192 offset:38912
	ds_read_b128 v[214:217], v192 offset:39936
	global_load_lds_dwordx4 v[224:225], off
	v_lshl_add_u64 v[224:225], s[38:39], 0, v[150:151]
	s_mov_b32 m0, s46
	s_nop 0
	global_load_lds_dwordx4 v[224:225], off
	s_waitcnt vmcnt(8)
	s_waitcnt lgkmcnt(0)
	s_setprio 1
	s_barrier
	s_waitcnt lgkmcnt(0)
	v_mfma_f32_16x16x32_bf16 v[126:129], v[130:133], v[178:181], v[126:129]
	v_mfma_f32_16x16x32_bf16 v[122:125], v[138:141], v[178:181], v[122:125]
	v_mfma_f32_16x16x32_bf16 v[110:113], v[130:133], v[194:197], v[110:113]
	v_mfma_f32_16x16x32_bf16 v[106:109], v[138:141], v[194:197], v[106:109]
	v_mfma_f32_16x16x32_bf16 v[94:97], v[130:133], v[202:205], v[94:97]
	v_mfma_f32_16x16x32_bf16 v[90:93], v[138:141], v[202:205], v[90:93]
	v_mfma_f32_16x16x32_bf16 v[78:81], v[130:133], v[210:213], v[78:81]
	v_mfma_f32_16x16x32_bf16 v[74:77], v[138:141], v[210:213], v[74:77]
	v_mfma_f32_16x16x32_bf16 v[126:129], v[134:137], v[182:185], v[126:129]
	v_mfma_f32_16x16x32_bf16 v[122:125], v[142:145], v[182:185], v[122:125]
	v_mfma_f32_16x16x32_bf16 v[110:113], v[134:137], v[198:201], v[110:113]
	v_mfma_f32_16x16x32_bf16 v[106:109], v[142:145], v[198:201], v[106:109]
	v_mfma_f32_16x16x32_bf16 v[94:97], v[134:137], v[206:209], v[94:97]
	v_mfma_f32_16x16x32_bf16 v[90:93], v[142:145], v[206:209], v[90:93]
	v_mfma_f32_16x16x32_bf16 v[78:81], v[134:137], v[214:217], v[78:81]
	v_mfma_f32_16x16x32_bf16 v[74:77], v[142:145], v[214:217], v[74:77]
	s_setprio 0
	s_setprio 1
	v_mfma_f32_16x16x32_bf16 v[118:121], v[162:165], v[178:181], v[118:121]
	v_mfma_f32_16x16x32_bf16 v[114:117], v[170:173], v[178:181], v[114:117]
	v_mfma_f32_16x16x32_bf16 v[102:105], v[162:165], v[194:197], v[102:105]
	v_mfma_f32_16x16x32_bf16 v[98:101], v[170:173], v[194:197], v[98:101]
	v_mfma_f32_16x16x32_bf16 v[86:89], v[162:165], v[202:205], v[86:89]
	v_mfma_f32_16x16x32_bf16 v[82:85], v[170:173], v[202:205], v[82:85]
	v_mfma_f32_16x16x32_bf16 v[70:73], v[162:165], v[210:213], v[70:73]
	v_mfma_f32_16x16x32_bf16 v[66:69], v[170:173], v[210:213], v[66:69]
	v_mfma_f32_16x16x32_bf16 v[118:121], v[166:169], v[182:185], v[118:121]
	v_mfma_f32_16x16x32_bf16 v[114:117], v[174:177], v[182:185], v[114:117]
	v_mfma_f32_16x16x32_bf16 v[102:105], v[166:169], v[198:201], v[102:105]
	v_mfma_f32_16x16x32_bf16 v[98:101], v[174:177], v[198:201], v[98:101]
	v_mfma_f32_16x16x32_bf16 v[86:89], v[166:169], v[206:209], v[86:89]
	v_mfma_f32_16x16x32_bf16 v[82:85], v[174:177], v[206:209], v[82:85]
	v_mfma_f32_16x16x32_bf16 v[70:73], v[166:169], v[214:217], v[70:73]
	v_mfma_f32_16x16x32_bf16 v[66:69], v[174:177], v[214:217], v[66:69]
	s_setprio 0
	s_barrier
; #define PG8_STAGE(bufoff, gbase, voff) do { _Pragma("unroll") for (int _i = 0; _i < 2; ++_i) \
;         __builtin_amdgcn_global_load_lds((const unsigned*)((const char*)(gbase) + (voff)[_i]), (PG8_LAS unsigned*)(lds + (bufoff) + ldsw + _i * 8192), 16, 0, 0); } while (0)
; #define PG8_LDA(dst, b, h) do { _Pragma("unroll") for (int m = 0; m < 4; ++m) _Pragma("unroll") for (int k = 0; k < 2; ++k) dst[m][k] = *(const PG8_LAS bf16x8*)(lds + PG8_SA(b, h) + aoff + m * 2048 + k * 1024); } while (0)
; #define PG8_WAIT_V(n) asm volatile("s_waitcnt vmcnt(" #n ")" ::: "memory")
; #define PG8_WAIT_L(n) asm volatile("s_waitcnt lgkmcnt(" #n ")" ::: "memory")
; #define PG8_BAR __builtin_amdgcn_s_barrier()
; #define PG8_SCHED __builtin_amdgcn_sched_barrier(0)
; template <class Epi, class Sched, bool ALIGN_EPI = false, bool SP2 = false, bool FP8 = false>
; __device__ __forceinline__ void gemm_phase(PG8_LAS unsigned char* lds, const Gemm g, const Sched& S, const Epi& E) {
;     ...
;             PG8_LDA(At, 1, 1); PG8_STAGE(PG8_SB(1, 0), b3, voffB); PG8_STAGE(PG8_SB(1, 1), b3 + hstep, voffB); PG8_STAGE(PG8_SA(1, 0), a3, voffA);
;             PG8_WAIT_V(8); PG8_WAIT_L(0); PG8_BAR; PG8_MMA(1, 0, At, B0); PG8_MMA(1, 1, At, B1); PG8_BAR; PG8_SCHED;
	s_add_i32 s38, s70, s43
	v_lshl_add_u64 v[186:187], v[186:187], 0, s[10:11]
	s_mov_b32 m0, s38
	ds_read_b128 v[178:181], v192 offset:49152
	ds_read_b128 v[182:185], v192 offset:50176
	ds_read_b128 v[194:197], v192 offset:51200
	ds_read_b128 v[198:201], v192 offset:52224
	ds_read_b128 v[202:205], v192 offset:53248
	ds_read_b128 v[206:209], v192 offset:54272
	ds_read_b128 v[210:213], v192 offset:55296
	ds_read_b128 v[214:217], v192 offset:56320
	global_load_lds_dwordx4 v[186:187], off
	s_add_i32 m0, s38, 0x2000
	s_add_u32 s36, s36, 0x80080
	v_lshl_add_u64 v[186:187], v[218:219], 0, s[10:11]
	s_addc_u32 s37, s37, 0
	s_add_i32 s38, s71, s43
	global_load_lds_dwordx4 v[186:187], off
	v_lshl_add_u64 v[186:187], s[36:37], 0, v[148:149]
	s_mov_b32 m0, s38
	s_nop 0
	global_load_lds_dwordx4 v[186:187], off
	v_lshl_add_u64 v[186:187], s[36:37], 0, v[152:153]
	s_add_i32 m0, s38, 0x2000
	s_nop 0
	global_load_lds_dwordx4 v[186:187], off
	v_lshl_add_u64 v[186:187], v[220:221], 0, s[10:11]
	s_mov_b32 m0, s51
	s_nop 0
	global_load_lds_dwordx4 v[186:187], off
	v_lshl_add_u64 v[186:187], v[222:223], 0, s[10:11]
	s_mov_b32 m0, s52
	s_nop 0
	global_load_lds_dwordx4 v[186:187], off
	s_waitcnt vmcnt(8)
	s_waitcnt lgkmcnt(0)
	s_setprio 1
	s_barrier
	s_waitcnt lgkmcnt(0)
	v_mfma_f32_16x16x32_bf16 v[62:65], v[130:133], v[178:181], v[62:65]
	v_mfma_f32_16x16x32_bf16 v[58:61], v[138:141], v[178:181], v[58:61]
	v_mfma_f32_16x16x32_bf16 v[46:49], v[130:133], v[194:197], v[46:49]
	v_mfma_f32_16x16x32_bf16 v[42:45], v[138:141], v[194:197], v[42:45]
	v_mfma_f32_16x16x32_bf16 v[30:33], v[130:133], v[202:205], v[30:33]
	v_mfma_f32_16x16x32_bf16 v[26:29], v[138:141], v[202:205], v[26:29]
	v_mfma_f32_16x16x32_bf16 v[14:17], v[130:133], v[210:213], v[14:17]
	v_mfma_f32_16x16x32_bf16 v[10:13], v[138:141], v[210:213], v[10:13]
	v_mfma_f32_16x16x32_bf16 v[62:65], v[134:137], v[182:185], v[62:65]
	v_mfma_f32_16x16x32_bf16 v[58:61], v[142:145], v[182:185], v[58:61]
	v_mfma_f32_16x16x32_bf16 v[46:49], v[134:137], v[198:201], v[46:49]
	v_mfma_f32_16x16x32_bf16 v[42:45], v[142:145], v[198:201], v[42:45]
	v_mfma_f32_16x16x32_bf16 v[30:33], v[134:137], v[206:209], v[30:33]
	v_mfma_f32_16x16x32_bf16 v[26:29], v[142:145], v[206:209], v[26:29]
	v_mfma_f32_16x16x32_bf16 v[14:17], v[134:137], v[214:217], v[14:17]
	v_mfma_f32_16x16x32_bf16 v[10:13], v[142:145], v[214:217], v[10:13]
	s_setprio 0
	s_setprio 1
	v_mfma_f32_16x16x32_bf16 v[54:57], v[162:165], v[178:181], v[54:57]
	v_mfma_f32_16x16x32_bf16 v[50:53], v[170:173], v[178:181], v[50:53]
	v_mfma_f32_16x16x32_bf16 v[38:41], v[162:165], v[194:197], v[38:41]
	v_mfma_f32_16x16x32_bf16 v[34:37], v[170:173], v[194:197], v[34:37]
	v_mfma_f32_16x16x32_bf16 v[22:25], v[162:165], v[202:205], v[22:25]
	v_mfma_f32_16x16x32_bf16 v[18:21], v[170:173], v[202:205], v[18:21]
	v_mfma_f32_16x16x32_bf16 v[6:9], v[162:165], v[210:213], v[6:9]
	v_mfma_f32_16x16x32_bf16 v[2:5], v[170:173], v[210:213], v[2:5]
	v_mfma_f32_16x16x32_bf16 v[54:57], v[166:169], v[182:185], v[54:57]
	v_mfma_f32_16x16x32_bf16 v[50:53], v[174:177], v[182:185], v[50:53]
	v_mfma_f32_16x16x32_bf16 v[38:41], v[166:169], v[198:201], v[38:41]
	v_mfma_f32_16x16x32_bf16 v[34:37], v[174:177], v[198:201], v[34:37]
	v_mfma_f32_16x16x32_bf16 v[22:25], v[166:169], v[206:209], v[22:25]
	v_mfma_f32_16x16x32_bf16 v[18:21], v[174:177], v[206:209], v[18:21]
	v_mfma_f32_16x16x32_bf16 v[6:9], v[166:169], v[214:217], v[6:9]
	v_mfma_f32_16x16x32_bf16 v[2:5], v[174:177], v[214:217], v[2:5]
	s_setprio 0
	s_add_i32 s69, s69, 2
	s_add_u32 s34, s34, 0x100
	s_addc_u32 s35, s35, 0
	s_add_u32 s63, s63, 0x100
	s_addc_u32 s68, s68, 0
	s_cmp_gt_u32 s69, 29
	s_barrier
	s_cbranch_scc0 .LBB0_1952
	s_and_b64 vcc, exec, s[12:13]
	s_cbranch_vccz .LBB0_1955
	s_barrier

; #define PG8_STAGE(bufoff, gbase, voff) do { _Pragma("unroll") for (int _i = 0; _i < 2; ++_i) \
;         __builtin_amdgcn_global_load_lds((const unsigned*)((const char*)(gbase) + (voff)[_i]), (PG8_LAS unsigned*)(lds + (bufoff) + ldsw + _i * 8192), 16, 0, 0); } while (0)
; #define PG8_LDA(dst, b, h) do { _Pragma("unroll") for (int m = 0; m < 4; ++m) _Pragma("unroll") for (int k = 0; k < 2; ++k) dst[m][k] = *(const PG8_LAS bf16x8*)(lds + PG8_SA(b, h) + aoff + m * 2048 + k * 1024); } while (0)
; #define PG8_LDB(dst, b, h) do { _Pragma("unroll") for (int n = 0; n < 2; ++n) _Pragma("unroll") for (int k = 0; k < 2; ++k) dst[n][k] = *(const PG8_LAS bf16x8*)(lds + PG8_SB(b, h) + boff + n * 2048 + k * 1024); } while (0)
; #define PG8_WAIT_V(n) asm volatile("s_waitcnt vmcnt(" #n ")" ::: "memory")
; #define PG8_WAIT_L(n) asm volatile("s_waitcnt lgkmcnt(" #n ")" ::: "memory")
; #define PG8_BAR __builtin_amdgcn_s_barrier()
; #define PG8_SCHED __builtin_amdgcn_sched_barrier(0)
; template <class Epi, class Sched, bool ALIGN_EPI = false, bool SP2 = false, bool FP8 = false>
; __device__ __forceinline__ void gemm_phase(PG8_LAS unsigned char* lds, const Gemm g, const Sched& S, const Epi& E) {
;     ...
;             const char* a1 = cA + (size_t)(t + 1) * kstep;
;             const char* a2 = last ? nA : cA + (size_t)(t + 2) * kstep; const char* b2 = last ? nB : cB + (size_t)(t + 2) * kstep;
;             const char* a3 = a2 + kstep; const char* b3 = b2 + kstep;
;             if (last && has_next) S.a_ready(nxt);
;             if constexpr (SP2) {
;             PG8_LDB(B0, 0, 0); PG8_LDB(B1, 0, 1); PG8_SCHED; PG8_LDA(At, 0, 0); PG8_STAGE(PG8_SA(1, 1), a1 + hstep, voffA);
;             PG8_WAIT_V(8); PG8_WAIT_L(0); PG8_BAR; PG8_MMA(0, 0, At, B0); PG8_MMA(0, 1, At, B1); PG8_BAR; PG8_SCHED;
;             PG8_LDA(At, 0, 1); PG8_STAGE(PG8_SB(0, 0), b2, voffB); PG8_STAGE(PG8_SB(0, 1), b2 + hstep, voffB); PG8_STAGE(PG8_SA(0, 0), a2, voffA);
;             PG8_WAIT_V(8); PG8_WAIT_L(0); PG8_BAR; PG8_MMA(1, 0, At, B0); PG8_MMA(1, 1, At, B1); PG8_BAR; PG8_SCHED;
.LBB0_2184:
	ds_read_b128 v[26:29], v184
	ds_read_b128 v[30:33], v184 offset:1024
	ds_read_b128 v[18:21], v184 offset:2048
	ds_read_b128 v[22:25], v184 offset:3072
	ds_read_b128 v[10:13], v185
	ds_read_b128 v[14:17], v185 offset:1024
	ds_read_b128 v[2:5], v185 offset:2048
	ds_read_b128 v[6:9], v185 offset:3072
	s_add_u32 s26, s24, 0xfffc0080
	s_addc_u32 s27, s25, -1
	s_cmp_eq_u32 s60, 12
	s_cselect_b32 s29, s13, s27
	s_cselect_b32 s28, s56, s26
	s_cselect_b32 s27, s17, s59
	s_cselect_b32 s26, s57, s58
	v_lshl_add_u64 v[212:213], s[24:25], 0, v[170:171]
	s_add_i32 m0, s23, 0xc000
	ds_read_b128 v[174:177], v186
	ds_read_b128 v[178:181], v186 offset:1024
	ds_read_b128 v[188:191], v186 offset:2048
	ds_read_b128 v[192:195], v186 offset:3072
	ds_read_b128 v[196:199], v186 offset:4096
	ds_read_b128 v[200:203], v186 offset:5120
	ds_read_b128 v[204:207], v186 offset:6144
	ds_read_b128 v[208:211], v186 offset:7168
	global_load_lds_dwordx4 v[212:213], off
	v_lshl_add_u64 v[212:213], s[24:25], 0, v[172:173]
	s_add_i32 m0, s23, 0xe000
	s_nop 0
	global_load_lds_dwordx4 v[212:213], off
	s_waitcnt vmcnt(8)
	s_waitcnt lgkmcnt(0)
	s_setprio 1
	s_barrier
	s_waitcnt lgkmcnt(0)
	v_mfma_f32_16x16x128_f8f6f4 v[158:161], v[26:33], v[174:181], v[158:161]
	v_mfma_f32_16x16x128_f8f6f4 v[150:153], v[18:25], v[174:181], v[150:153]
	v_mfma_f32_16x16x128_f8f6f4 v[142:145], v[26:33], v[188:195], v[142:145]
	v_mfma_f32_16x16x128_f8f6f4 v[134:137], v[18:25], v[188:195], v[134:137]
	v_mfma_f32_16x16x128_f8f6f4 v[126:129], v[26:33], v[196:203], v[126:129]
	v_mfma_f32_16x16x128_f8f6f4 v[118:121], v[18:25], v[196:203], v[118:121]
	v_mfma_f32_16x16x128_f8f6f4 v[110:113], v[26:33], v[204:211], v[110:113]
	v_mfma_f32_16x16x128_f8f6f4 v[102:105], v[18:25], v[204:211], v[102:105]
	s_setprio 0
	s_setprio 1
	v_mfma_f32_16x16x128_f8f6f4 v[154:157], v[10:17], v[174:181], v[154:157]
	v_mfma_f32_16x16x128_f8f6f4 v[146:149], v[2:9], v[174:181], v[146:149]
	v_mfma_f32_16x16x128_f8f6f4 v[138:141], v[10:17], v[188:195], v[138:141]
	v_mfma_f32_16x16x128_f8f6f4 v[130:133], v[2:9], v[188:195], v[130:133]
	v_mfma_f32_16x16x128_f8f6f4 v[122:125], v[10:17], v[196:203], v[122:125]
	v_mfma_f32_16x16x128_f8f6f4 v[114:117], v[2:9], v[196:203], v[114:117]
	v_mfma_f32_16x16x128_f8f6f4 v[106:109], v[10:17], v[204:211], v[106:109]
	v_mfma_f32_16x16x128_f8f6f4 v[98:101], v[2:9], v[204:211], v[98:101]
	s_setprio 0
	s_barrier
	s_add_i32 s61, s51, s43
	v_lshl_add_u64 v[174:175], s[26:27], 0, v[162:163]
	s_mov_b32 m0, s61
	ds_read_b128 v[188:191], v186 offset:16384
	ds_read_b128 v[192:195], v186 offset:17408
	ds_read_b128 v[196:199], v186 offset:18432
	ds_read_b128 v[200:203], v186 offset:19456
	ds_read_b128 v[204:207], v186 offset:20480
	ds_read_b128 v[208:211], v186 offset:21504
	ds_read_b128 v[212:215], v186 offset:22528
	ds_read_b128 v[216:219], v186 offset:23552
	global_load_lds_dwordx4 v[174:175], off
	s_add_i32 m0, s61, 0x2000
	s_add_u32 s62, s26, 0x40000
	v_lshl_add_u64 v[176:177], s[26:27], 0, v[164:165]
	s_addc_u32 s63, s27, 0
	s_add_i32 s61, s52, s43
	global_load_lds_dwordx4 v[176:177], off
	v_lshl_add_u64 v[178:179], s[62:63], 0, v[162:163]
	s_mov_b32 m0, s61
	v_lshl_add_u64 v[180:181], s[28:29], 0, v[166:167]
	global_load_lds_dwordx4 v[178:179], off
	v_lshl_add_u64 v[178:179], s[62:63], 0, v[164:165]
	s_add_i32 m0, s61, 0x2000
	s_nop 0
	global_load_lds_dwordx4 v[178:179], off
	v_lshl_add_u64 v[178:179], s[28:29], 0, v[168:169]
	s_mov_b32 m0, s23
	s_nop 0
	global_load_lds_dwordx4 v[178:179], off
	s_mov_b32 m0, s44
	s_nop 0
	global_load_lds_dwordx4 v[180:181], off
	s_waitcnt vmcnt(8)
	s_waitcnt lgkmcnt(0)
	s_setprio 1
	s_barrier
	s_waitcnt lgkmcnt(0)
	v_mfma_f32_16x16x128_f8f6f4 v[94:97], v[26:33], v[188:195], v[94:97]
	v_mfma_f32_16x16x128_f8f6f4 v[86:89], v[18:25], v[188:195], v[86:89]
	v_mfma_f32_16x16x128_f8f6f4 v[78:81], v[26:33], v[196:203], v[78:81]
	v_mfma_f32_16x16x128_f8f6f4 v[70:73], v[18:25], v[196:203], v[70:73]
	v_mfma_f32_16x16x128_f8f6f4 v[62:65], v[26:33], v[204:211], v[62:65]
	v_mfma_f32_16x16x128_f8f6f4 v[54:57], v[18:25], v[204:211], v[54:57]
	v_mfma_f32_16x16x128_f8f6f4 v[46:49], v[26:33], v[212:219], v[46:49]
	v_mfma_f32_16x16x128_f8f6f4 v[38:41], v[18:25], v[212:219], v[38:41]
	s_setprio 0
	s_setprio 1
	v_mfma_f32_16x16x128_f8f6f4 v[90:93], v[10:17], v[188:195], v[90:93]
	v_mfma_f32_16x16x128_f8f6f4 v[82:85], v[2:9], v[188:195], v[82:85]
	v_mfma_f32_16x16x128_f8f6f4 v[74:77], v[10:17], v[196:203], v[74:77]
	v_mfma_f32_16x16x128_f8f6f4 v[66:69], v[2:9], v[196:203], v[66:69]
	v_mfma_f32_16x16x128_f8f6f4 v[58:61], v[10:17], v[204:211], v[58:61]
	v_mfma_f32_16x16x128_f8f6f4 v[50:53], v[2:9], v[204:211], v[50:53]
	v_mfma_f32_16x16x128_f8f6f4 v[42:45], v[10:17], v[212:219], v[42:45]
	v_mfma_f32_16x16x128_f8f6f4 v[34:37], v[2:9], v[212:219], v[34:37]
	s_setprio 0
	s_barrier
; #define PG8_STAGE(bufoff, gbase, voff) do { _Pragma("unroll") for (int _i = 0; _i < 2; ++_i) \
;         __builtin_amdgcn_global_load_lds((const unsigned*)((const char*)(gbase) + (voff)[_i]), (PG8_LAS unsigned*)(lds + (bufoff) + ldsw + _i * 8192), 16, 0, 0); } while (0)
; #define PG8_LDA(dst, b, h) do { _Pragma("unroll") for (int m = 0; m < 4; ++m) _Pragma("unroll") for (int k = 0; k < 2; ++k) dst[m][k] = *(const PG8_LAS bf16x8*)(lds + PG8_SA(b, h) + aoff + m * 2048 + k * 1024); } while (0)
; #define PG8_LDB(dst, b, h) do { _Pragma("unroll") for (int n = 0; n < 2; ++n) _Pragma("unroll") for (int k = 0; k < 2; ++k) dst[n][k] = *(const PG8_LAS bf16x8*)(lds + PG8_SB(b, h) + boff + n * 2048 + k * 1024); } while (0)
; #define PG8_WAIT_V(n) asm volatile("s_waitcnt vmcnt(" #n ")" ::: "memory")
; #define PG8_WAIT_L(n) asm volatile("s_waitcnt lgkmcnt(" #n ")" ::: "memory")
; #define PG8_BAR __builtin_amdgcn_s_barrier()
; #define PG8_SCHED __builtin_amdgcn_sched_barrier(0)
; template <class Epi, class Sched, bool ALIGN_EPI = false, bool SP2 = false, bool FP8 = false>
; __device__ __forceinline__ void gemm_phase(PG8_LAS unsigned char* lds, const Gemm g, const Sched& S, const Epi& E) {
;     ...
;             PG8_LDB(B0, 1, 0); PG8_LDB(B1, 1, 1); PG8_SCHED; PG8_LDA(At, 1, 0); PG8_STAGE(PG8_SA(0, 1), a2 + hstep, voffA);
;             PG8_WAIT_V(8); PG8_WAIT_L(0); PG8_BAR; PG8_MMA(0, 0, At, B0); PG8_MMA(0, 1, At, B1); PG8_BAR; PG8_SCHED;
;             PG8_LDA(At, 1, 1); PG8_STAGE(PG8_SB(1, 0), b3, voffB); PG8_STAGE(PG8_SB(1, 1), b3 + hstep, voffB); PG8_STAGE(PG8_SA(1, 0), a3, voffA);
;             PG8_WAIT_V(8); PG8_WAIT_L(0); PG8_BAR; PG8_MMA(1, 0, At, B0); PG8_MMA(1, 1, At, B1); PG8_BAR; PG8_SCHED;
	s_add_i32 s61, 0, 0x18000
	s_add_i32 s62, 0, 0x1c000
	v_add_u32_e32 v14, s61, v182
	v_add_u32_e32 v30, s62, v182
	ds_read_b128 v[2:5], v14
	ds_read_b128 v[6:9], v14 offset:1024
	ds_read_b128 v[10:13], v14 offset:2048
	ds_read_b128 v[14:17], v14 offset:3072
	ds_read_b128 v[18:21], v30
	ds_read_b128 v[22:25], v30 offset:1024
	ds_read_b128 v[26:29], v30 offset:2048
	ds_read_b128 v[30:33], v30 offset:3072
	s_add_u32 s28, s28, 0x40000
	s_addc_u32 s29, s29, 0
	s_mov_b32 m0, s45
	v_lshl_add_u64 v[220:221], s[28:29], 0, v[168:169]
	ds_read_b128 v[188:191], v186 offset:32768
	ds_read_b128 v[192:195], v186 offset:33792
	ds_read_b128 v[196:199], v186 offset:34816
	ds_read_b128 v[200:203], v186 offset:35840
	ds_read_b128 v[204:207], v186 offset:36864
	ds_read_b128 v[208:211], v186 offset:37888
	ds_read_b128 v[212:215], v186 offset:38912
	ds_read_b128 v[216:219], v186 offset:39936
	global_load_lds_dwordx4 v[220:221], off
	v_lshl_add_u64 v[220:221], s[28:29], 0, v[166:167]
	s_mov_b32 m0, s46
	s_nop 0
	global_load_lds_dwordx4 v[220:221], off
	s_waitcnt vmcnt(8)
	s_waitcnt lgkmcnt(0)
	s_setprio 1
	s_barrier
	s_waitcnt lgkmcnt(0)
	v_mfma_f32_16x16x128_f8f6f4 v[158:161], v[2:9], v[188:195], v[158:161]
	v_mfma_f32_16x16x128_f8f6f4 v[150:153], v[10:17], v[188:195], v[150:153]
	v_mfma_f32_16x16x128_f8f6f4 v[142:145], v[2:9], v[196:203], v[142:145]
	v_mfma_f32_16x16x128_f8f6f4 v[134:137], v[10:17], v[196:203], v[134:137]
	v_mfma_f32_16x16x128_f8f6f4 v[126:129], v[2:9], v[204:211], v[126:129]
	v_mfma_f32_16x16x128_f8f6f4 v[118:121], v[10:17], v[204:211], v[118:121]
	v_mfma_f32_16x16x128_f8f6f4 v[110:113], v[2:9], v[212:219], v[110:113]
	v_mfma_f32_16x16x128_f8f6f4 v[102:105], v[10:17], v[212:219], v[102:105]
	s_setprio 0
	s_setprio 1
	v_mfma_f32_16x16x128_f8f6f4 v[154:157], v[18:25], v[188:195], v[154:157]
	v_mfma_f32_16x16x128_f8f6f4 v[146:149], v[26:33], v[188:195], v[146:149]
	v_mfma_f32_16x16x128_f8f6f4 v[138:141], v[18:25], v[196:203], v[138:141]
	v_mfma_f32_16x16x128_f8f6f4 v[130:133], v[26:33], v[196:203], v[130:133]
	v_mfma_f32_16x16x128_f8f6f4 v[122:125], v[18:25], v[204:211], v[122:125]
	v_mfma_f32_16x16x128_f8f6f4 v[114:117], v[26:33], v[204:211], v[114:117]
	v_mfma_f32_16x16x128_f8f6f4 v[106:109], v[18:25], v[212:219], v[106:109]
	v_mfma_f32_16x16x128_f8f6f4 v[98:101], v[26:33], v[212:219], v[98:101]
	s_setprio 0
	s_barrier
	s_add_i32 s28, s61, s43
	v_lshl_add_u64 v[174:175], v[174:175], 0, s[6:7]
	s_mov_b32 m0, s28
	ds_read_b128 v[188:191], v186 offset:49152
	ds_read_b128 v[192:195], v186 offset:50176
	ds_read_b128 v[196:199], v186 offset:51200
	ds_read_b128 v[200:203], v186 offset:52224
	ds_read_b128 v[204:207], v186 offset:53248
	ds_read_b128 v[208:211], v186 offset:54272
	ds_read_b128 v[212:215], v186 offset:55296
	ds_read_b128 v[216:219], v186 offset:56320
	global_load_lds_dwordx4 v[174:175], off
	s_add_i32 m0, s28, 0x2000
	s_add_u32 s26, s26, 0x40080
	v_lshl_add_u64 v[174:175], v[176:177], 0, s[6:7]
	s_addc_u32 s27, s27, 0
	s_add_i32 s28, s62, s43
	global_load_lds_dwordx4 v[174:175], off
	v_lshl_add_u64 v[174:175], s[26:27], 0, v[162:163]
	s_mov_b32 m0, s28
	s_nop 0
	global_load_lds_dwordx4 v[174:175], off
	v_lshl_add_u64 v[174:175], s[26:27], 0, v[164:165]
	s_add_i32 m0, s28, 0x2000
	s_nop 0
	global_load_lds_dwordx4 v[174:175], off
	v_lshl_add_u64 v[174:175], v[178:179], 0, s[6:7]
	s_mov_b32 m0, s49
	s_nop 0
	global_load_lds_dwordx4 v[174:175], off
	v_lshl_add_u64 v[174:175], v[180:181], 0, s[6:7]
	s_mov_b32 m0, s50
	s_nop 0
	global_load_lds_dwordx4 v[174:175], off
	s_waitcnt vmcnt(8)
	s_waitcnt lgkmcnt(0)
	s_setprio 1
	s_barrier
	s_waitcnt lgkmcnt(0)
	v_mfma_f32_16x16x128_f8f6f4 v[94:97], v[2:9], v[188:195], v[94:97]
	v_mfma_f32_16x16x128_f8f6f4 v[86:89], v[10:17], v[188:195], v[86:89]
	v_mfma_f32_16x16x128_f8f6f4 v[78:81], v[2:9], v[196:203], v[78:81]
	v_mfma_f32_16x16x128_f8f6f4 v[70:73], v[10:17], v[196:203], v[70:73]
	v_mfma_f32_16x16x128_f8f6f4 v[62:65], v[2:9], v[204:211], v[62:65]
	v_mfma_f32_16x16x128_f8f6f4 v[54:57], v[10:17], v[204:211], v[54:57]
	v_mfma_f32_16x16x128_f8f6f4 v[46:49], v[2:9], v[212:219], v[46:49]
	v_mfma_f32_16x16x128_f8f6f4 v[38:41], v[10:17], v[212:219], v[38:41]
	s_setprio 0
	s_setprio 1
	v_mfma_f32_16x16x128_f8f6f4 v[90:93], v[18:25], v[188:195], v[90:93]
	v_mfma_f32_16x16x128_f8f6f4 v[82:85], v[26:33], v[188:195], v[82:85]
	v_mfma_f32_16x16x128_f8f6f4 v[74:77], v[18:25], v[196:203], v[74:77]
	v_mfma_f32_16x16x128_f8f6f4 v[66:69], v[26:33], v[196:203], v[66:69]
	v_mfma_f32_16x16x128_f8f6f4 v[58:61], v[18:25], v[204:211], v[58:61]
	v_mfma_f32_16x16x128_f8f6f4 v[50:53], v[26:33], v[204:211], v[50:53]
	v_mfma_f32_16x16x128_f8f6f4 v[42:45], v[18:25], v[212:219], v[42:45]
	v_mfma_f32_16x16x128_f8f6f4 v[34:37], v[26:33], v[212:219], v[34:37]
	s_setprio 0
	s_add_i32 s60, s60, 2
	s_add_u32 s24, s24, 0x100
	s_addc_u32 s25, s25, 0
	s_add_u32 s58, s58, 0x100
	s_addc_u32 s59, s59, 0
	s_cmp_gt_u32 s60, 13
	s_barrier
	s_cbranch_scc0 .LBB0_2184
	s_nop 15
	s_nop 15
	s_nop 15
	s_nop 15
	s_and_b64 vcc, exec, s[8:9]
	s_cbranch_vccz .LBB0_2187
	s_barrier

; #define PG8_STAGE(bufoff, gbase, voff) do { _Pragma("unroll") for (int _i = 0; _i < 2; ++_i) \
;         __builtin_amdgcn_global_load_lds((const unsigned*)((const char*)(gbase) + (voff)[_i]), (PG8_LAS unsigned*)(lds + (bufoff) + ldsw + _i * 8192), 16, 0, 0); } while (0)
; #define PG8_LDA(dst, b, h) do { _Pragma("unroll") for (int m = 0; m < 4; ++m) _Pragma("unroll") for (int k = 0; k < 2; ++k) dst[m][k] = *(const PG8_LAS bf16x8*)(lds + PG8_SA(b, h) + aoff + m * 2048 + k * 1024); } while (0)
; #define PG8_LDB(dst, b, h) do { _Pragma("unroll") for (int n = 0; n < 2; ++n) _Pragma("unroll") for (int k = 0; k < 2; ++k) dst[n][k] = *(const PG8_LAS bf16x8*)(lds + PG8_SB(b, h) + boff + n * 2048 + k * 1024); } while (0)
; #define PG8_WAIT_V(n) asm volatile("s_waitcnt vmcnt(" #n ")" ::: "memory")
; #define PG8_WAIT_L(n) asm volatile("s_waitcnt lgkmcnt(" #n ")" ::: "memory")
; #define PG8_BAR __builtin_amdgcn_s_barrier()
; #define PG8_SCHED __builtin_amdgcn_sched_barrier(0)
; template <class Epi, class Sched, bool ALIGN_EPI = false, bool SP2 = false, bool FP8 = false>
; __device__ __forceinline__ void gemm_phase(PG8_LAS unsigned char* lds, const Gemm g, const Sched& S, const Epi& E) {
;     ...
;             const char* a1 = cA + (size_t)(t + 1) * kstep;
;             const char* a2 = last ? nA : cA + (size_t)(t + 2) * kstep; const char* b2 = last ? nB : cB + (size_t)(t + 2) * kstep;
;             const char* a3 = a2 + kstep; const char* b3 = b2 + kstep;
;             if (last && has_next) S.a_ready(nxt);
;             if constexpr (SP2) {
;             PG8_LDB(B0, 0, 0); PG8_LDB(B1, 0, 1); PG8_SCHED; PG8_LDA(At, 0, 0); PG8_STAGE(PG8_SA(1, 1), a1 + hstep, voffA);
;             PG8_WAIT_V(8); PG8_WAIT_L(0); PG8_BAR; PG8_MMA(0, 0, At, B0); PG8_MMA(0, 1, At, B1); PG8_BAR; PG8_SCHED;
;             PG8_LDA(At, 0, 1); PG8_STAGE(PG8_SB(0, 0), b2, voffB); PG8_STAGE(PG8_SB(0, 1), b2 + hstep, voffB); PG8_STAGE(PG8_SA(0, 0), a2, voffA);
;             PG8_WAIT_V(8); PG8_WAIT_L(0); PG8_BAR; PG8_MMA(1, 0, At, B0); PG8_MMA(1, 1, At, B1); PG8_BAR; PG8_SCHED;
.LBB0_2259:
	ds_read_b128 v[26:29], v186
	ds_read_b128 v[30:33], v186 offset:1024
	ds_read_b128 v[18:21], v186 offset:2048
	ds_read_b128 v[22:25], v186 offset:3072
	ds_read_b128 v[10:13], v187
	ds_read_b128 v[14:17], v187 offset:1024
	ds_read_b128 v[2:5], v187 offset:2048
	ds_read_b128 v[6:9], v187 offset:3072
	s_add_u32 s36, s34, 0xfff20080
	s_addc_u32 s37, s35, -1
	s_cmp_eq_u32 s71, 52
	s_cselect_b64 vcc, -1, 0
	s_cselect_b32 s37, s31, s37
	s_cselect_b32 s36, s30, s36
	v_cndmask_b32_e32 v175, v173, v171, vcc
	v_cndmask_b32_e32 v174, v172, v170, vcc
	v_lshl_add_u64 v[214:215], s[34:35], 0, v[166:167]
	s_add_i32 m0, s48, 0xc000
	ds_read_b128 v[176:179], v188
	ds_read_b128 v[180:183], v188 offset:1024
	ds_read_b128 v[190:193], v188 offset:2048
	ds_read_b128 v[194:197], v188 offset:3072
	ds_read_b128 v[198:201], v188 offset:4096
	ds_read_b128 v[202:205], v188 offset:5120
	ds_read_b128 v[206:209], v188 offset:6144
	ds_read_b128 v[210:213], v188 offset:7168
	global_load_lds_dwordx4 v[214:215], off
	v_lshl_add_u64 v[214:215], s[34:35], 0, v[168:169]
	s_add_i32 m0, s48, 0xe000
	s_nop 0
	global_load_lds_dwordx4 v[214:215], off
	s_waitcnt vmcnt(8)
	s_waitcnt lgkmcnt(0)
	s_setprio 1
	s_barrier
	s_waitcnt lgkmcnt(0)
	v_mfma_f32_16x16x128_f8f6f4 v[158:161], v[26:33], v[176:183], v[158:161]
	v_mfma_f32_16x16x128_f8f6f4 v[154:157], v[18:25], v[176:183], v[154:157]
	v_mfma_f32_16x16x128_f8f6f4 v[146:149], v[26:33], v[190:197], v[146:149]
	v_mfma_f32_16x16x128_f8f6f4 v[138:141], v[18:25], v[190:197], v[138:141]
	v_mfma_f32_16x16x128_f8f6f4 v[130:133], v[26:33], v[198:205], v[130:133]
	v_mfma_f32_16x16x128_f8f6f4 v[122:125], v[18:25], v[198:205], v[122:125]
	v_mfma_f32_16x16x128_f8f6f4 v[114:117], v[26:33], v[206:213], v[114:117]
	v_mfma_f32_16x16x128_f8f6f4 v[106:109], v[18:25], v[206:213], v[106:109]
	s_setprio 0
	s_setprio 1
	v_mfma_f32_16x16x128_f8f6f4 v[150:153], v[10:17], v[176:183], v[150:153]
	v_mfma_f32_16x16x128_f8f6f4 v[142:145], v[2:9], v[176:183], v[142:145]
	v_mfma_f32_16x16x128_f8f6f4 v[134:137], v[10:17], v[190:197], v[134:137]
	v_mfma_f32_16x16x128_f8f6f4 v[126:129], v[2:9], v[190:197], v[126:129]
	v_mfma_f32_16x16x128_f8f6f4 v[118:121], v[10:17], v[198:205], v[118:121]
	v_mfma_f32_16x16x128_f8f6f4 v[110:113], v[2:9], v[198:205], v[110:113]
	v_mfma_f32_16x16x128_f8f6f4 v[102:105], v[10:17], v[206:213], v[102:105]
	v_mfma_f32_16x16x128_f8f6f4 v[98:101], v[2:9], v[206:213], v[98:101]
	s_setprio 0
	s_barrier
	s_add_i32 s72, s57, s47
	v_lshl_add_u64 v[176:177], v[174:175], 0, v[162:163]
	s_mov_b32 m0, s72
	ds_read_b128 v[190:193], v188 offset:16384
	ds_read_b128 v[194:197], v188 offset:17408
	ds_read_b128 v[198:201], v188 offset:18432
	ds_read_b128 v[202:205], v188 offset:19456
	ds_read_b128 v[206:209], v188 offset:20480
	ds_read_b128 v[210:213], v188 offset:21504
	ds_read_b128 v[214:217], v188 offset:22528
	ds_read_b128 v[218:221], v188 offset:23552
	global_load_lds_dwordx4 v[176:177], off
	v_lshl_add_u64 v[178:179], v[174:175], 0, v[164:165]
	s_add_i32 m0, s72, 0x2000
	v_lshl_add_u64 v[180:181], v[174:175], 0, s[6:7]
	s_add_i32 s72, s58, s47
	global_load_lds_dwordx4 v[178:179], off
	v_lshl_add_u64 v[182:183], v[180:181], 0, v[162:163]
	s_mov_b32 m0, s72
	v_lshl_add_u64 v[180:181], v[180:181], 0, v[164:165]
	global_load_lds_dwordx4 v[182:183], off
	s_add_i32 m0, s72, 0x2000
	v_lshl_add_u64 v[182:183], s[36:37], 0, v[164:165]
	global_load_lds_dwordx4 v[180:181], off
	v_lshl_add_u64 v[180:181], s[36:37], 0, v[162:163]
	s_mov_b32 m0, s48
	s_nop 0
	global_load_lds_dwordx4 v[180:181], off
	s_mov_b32 m0, s49
	s_nop 0
	global_load_lds_dwordx4 v[182:183], off
	s_waitcnt vmcnt(8)
	s_waitcnt lgkmcnt(0)
	s_setprio 1
	s_barrier
	s_waitcnt lgkmcnt(0)
	v_mfma_f32_16x16x128_f8f6f4 v[94:97], v[26:33], v[190:197], v[94:97]
	v_mfma_f32_16x16x128_f8f6f4 v[90:93], v[18:25], v[190:197], v[90:93]
	v_mfma_f32_16x16x128_f8f6f4 v[82:85], v[26:33], v[198:205], v[82:85]
	v_mfma_f32_16x16x128_f8f6f4 v[74:77], v[18:25], v[198:205], v[74:77]
	v_mfma_f32_16x16x128_f8f6f4 v[66:69], v[26:33], v[206:213], v[66:69]
	v_mfma_f32_16x16x128_f8f6f4 v[58:61], v[18:25], v[206:213], v[58:61]
	v_mfma_f32_16x16x128_f8f6f4 v[50:53], v[26:33], v[214:221], v[50:53]
	v_mfma_f32_16x16x128_f8f6f4 v[42:45], v[18:25], v[214:221], v[42:45]
	s_setprio 0
	s_setprio 1
	v_mfma_f32_16x16x128_f8f6f4 v[86:89], v[10:17], v[190:197], v[86:89]
	v_mfma_f32_16x16x128_f8f6f4 v[78:81], v[2:9], v[190:197], v[78:81]
	v_mfma_f32_16x16x128_f8f6f4 v[70:73], v[10:17], v[198:205], v[70:73]
	v_mfma_f32_16x16x128_f8f6f4 v[62:65], v[2:9], v[198:205], v[62:65]
	v_mfma_f32_16x16x128_f8f6f4 v[54:57], v[10:17], v[206:213], v[54:57]
	v_mfma_f32_16x16x128_f8f6f4 v[46:49], v[2:9], v[206:213], v[46:49]
	v_mfma_f32_16x16x128_f8f6f4 v[38:41], v[10:17], v[214:221], v[38:41]
	v_mfma_f32_16x16x128_f8f6f4 v[34:37], v[2:9], v[214:221], v[34:37]
	s_setprio 0
	s_barrier
; #define PG8_STAGE(bufoff, gbase, voff) do { _Pragma("unroll") for (int _i = 0; _i < 2; ++_i) \
;         __builtin_amdgcn_global_load_lds((const unsigned*)((const char*)(gbase) + (voff)[_i]), (PG8_LAS unsigned*)(lds + (bufoff) + ldsw + _i * 8192), 16, 0, 0); } while (0)
; #define PG8_LDA(dst, b, h) do { _Pragma("unroll") for (int m = 0; m < 4; ++m) _Pragma("unroll") for (int k = 0; k < 2; ++k) dst[m][k] = *(const PG8_LAS bf16x8*)(lds + PG8_SA(b, h) + aoff + m * 2048 + k * 1024); } while (0)
; #define PG8_LDB(dst, b, h) do { _Pragma("unroll") for (int n = 0; n < 2; ++n) _Pragma("unroll") for (int k = 0; k < 2; ++k) dst[n][k] = *(const PG8_LAS bf16x8*)(lds + PG8_SB(b, h) + boff + n * 2048 + k * 1024); } while (0)
; #define PG8_WAIT_V(n) asm volatile("s_waitcnt vmcnt(" #n ")" ::: "memory")
; #define PG8_WAIT_L(n) asm volatile("s_waitcnt lgkmcnt(" #n ")" ::: "memory")
; #define PG8_BAR __builtin_amdgcn_s_barrier()
; #define PG8_SCHED __builtin_amdgcn_sched_barrier(0)
; template <class Epi, class Sched, bool ALIGN_EPI = false, bool SP2 = false, bool FP8 = false>
; __device__ __forceinline__ void gemm_phase(PG8_LAS unsigned char* lds, const Gemm g, const Sched& S, const Epi& E) {
;     ...
;             PG8_LDB(B0, 1, 0); PG8_LDB(B1, 1, 1); PG8_SCHED; PG8_LDA(At, 1, 0); PG8_STAGE(PG8_SA(0, 1), a2 + hstep, voffA);
;             PG8_WAIT_V(8); PG8_WAIT_L(0); PG8_BAR; PG8_MMA(0, 0, At, B0); PG8_MMA(0, 1, At, B1); PG8_BAR; PG8_SCHED;
;             PG8_LDA(At, 1, 1); PG8_STAGE(PG8_SB(1, 0), b3, voffB); PG8_STAGE(PG8_SB(1, 1), b3 + hstep, voffB); PG8_STAGE(PG8_SA(1, 0), a3, voffA);
;             PG8_WAIT_V(8); PG8_WAIT_L(0); PG8_BAR; PG8_MMA(1, 0, At, B0); PG8_MMA(1, 1, At, B1); PG8_BAR; PG8_SCHED;
	s_add_i32 s72, 0, 0x18000
	s_add_i32 s73, 0, 0x1c000
	v_add_u32_e32 v14, s72, v184
	v_add_u32_e32 v30, s73, v184
	ds_read_b128 v[2:5], v14
	ds_read_b128 v[6:9], v14 offset:1024
	ds_read_b128 v[10:13], v14 offset:2048
	ds_read_b128 v[14:17], v14 offset:3072
	ds_read_b128 v[18:21], v30
	ds_read_b128 v[22:25], v30 offset:1024
	ds_read_b128 v[26:29], v30 offset:2048
	ds_read_b128 v[30:33], v30 offset:3072
	s_add_u32 s36, s36, 0xe0000
	s_addc_u32 s37, s37, 0
	s_mov_b32 m0, s50
	v_lshl_add_u64 v[222:223], s[36:37], 0, v[162:163]
	ds_read_b128 v[190:193], v188 offset:32768
	ds_read_b128 v[194:197], v188 offset:33792
	ds_read_b128 v[198:201], v188 offset:34816
	ds_read_b128 v[202:205], v188 offset:35840
	ds_read_b128 v[206:209], v188 offset:36864
	ds_read_b128 v[210:213], v188 offset:37888
	ds_read_b128 v[214:217], v188 offset:38912
	ds_read_b128 v[218:221], v188 offset:39936
	global_load_lds_dwordx4 v[222:223], off
	v_lshl_add_u64 v[222:223], s[36:37], 0, v[164:165]
	s_mov_b32 m0, s51
	s_nop 0
	global_load_lds_dwordx4 v[222:223], off
	s_waitcnt vmcnt(8)
	s_waitcnt lgkmcnt(0)
	s_setprio 1
	s_barrier
	s_waitcnt lgkmcnt(0)
	v_mfma_f32_16x16x128_f8f6f4 v[158:161], v[2:9], v[190:197], v[158:161]
	v_mfma_f32_16x16x128_f8f6f4 v[154:157], v[10:17], v[190:197], v[154:157]
	v_mfma_f32_16x16x128_f8f6f4 v[146:149], v[2:9], v[198:205], v[146:149]
	v_mfma_f32_16x16x128_f8f6f4 v[138:141], v[10:17], v[198:205], v[138:141]
	v_mfma_f32_16x16x128_f8f6f4 v[130:133], v[2:9], v[206:213], v[130:133]
	v_mfma_f32_16x16x128_f8f6f4 v[122:125], v[10:17], v[206:213], v[122:125]
	v_mfma_f32_16x16x128_f8f6f4 v[114:117], v[2:9], v[214:221], v[114:117]
	v_mfma_f32_16x16x128_f8f6f4 v[106:109], v[10:17], v[214:221], v[106:109]
	s_setprio 0
	s_setprio 1
	v_mfma_f32_16x16x128_f8f6f4 v[150:153], v[18:25], v[190:197], v[150:153]
	v_mfma_f32_16x16x128_f8f6f4 v[142:145], v[26:33], v[190:197], v[142:145]
	v_mfma_f32_16x16x128_f8f6f4 v[134:137], v[18:25], v[198:205], v[134:137]
	v_mfma_f32_16x16x128_f8f6f4 v[126:129], v[26:33], v[198:205], v[126:129]
	v_mfma_f32_16x16x128_f8f6f4 v[118:121], v[18:25], v[206:213], v[118:121]
	v_mfma_f32_16x16x128_f8f6f4 v[110:113], v[26:33], v[206:213], v[110:113]
	v_mfma_f32_16x16x128_f8f6f4 v[102:105], v[18:25], v[214:221], v[102:105]
	v_mfma_f32_16x16x128_f8f6f4 v[98:101], v[26:33], v[214:221], v[98:101]
	s_setprio 0
	s_barrier
	s_add_i32 s36, s72, s47
	v_lshl_add_u64 v[176:177], v[176:177], 0, s[12:13]
	s_mov_b32 m0, s36
	ds_read_b128 v[190:193], v188 offset:49152
	ds_read_b128 v[194:197], v188 offset:50176
	ds_read_b128 v[198:201], v188 offset:51200
	ds_read_b128 v[202:205], v188 offset:52224
	ds_read_b128 v[206:209], v188 offset:53248
	ds_read_b128 v[210:213], v188 offset:54272
	ds_read_b128 v[214:217], v188 offset:55296
	ds_read_b128 v[218:221], v188 offset:56320
	global_load_lds_dwordx4 v[176:177], off
	v_lshl_add_u64 v[176:177], v[178:179], 0, s[12:13]
	s_add_i32 m0, s36, 0x2000
	v_lshl_add_u64 v[174:175], v[174:175], 0, s[14:15]
	s_add_i32 s36, s73, s47
	global_load_lds_dwordx4 v[176:177], off
	v_lshl_add_u64 v[176:177], v[174:175], 0, v[162:163]
	s_mov_b32 m0, s36
	v_lshl_add_u64 v[174:175], v[174:175], 0, v[164:165]
	global_load_lds_dwordx4 v[176:177], off
	s_add_i32 m0, s36, 0x2000
	s_nop 0
	global_load_lds_dwordx4 v[174:175], off
	v_lshl_add_u64 v[174:175], v[180:181], 0, s[12:13]
	s_mov_b32 m0, s55
	s_nop 0
	global_load_lds_dwordx4 v[174:175], off
	v_lshl_add_u64 v[174:175], v[182:183], 0, s[12:13]
	s_mov_b32 m0, s56
	s_nop 0
	global_load_lds_dwordx4 v[174:175], off
	s_waitcnt vmcnt(8)
	s_waitcnt lgkmcnt(0)
	s_setprio 1
	s_barrier
	s_waitcnt lgkmcnt(0)
	v_mfma_f32_16x16x128_f8f6f4 v[94:97], v[2:9], v[190:197], v[94:97]
	v_mfma_f32_16x16x128_f8f6f4 v[90:93], v[10:17], v[190:197], v[90:93]
	v_mfma_f32_16x16x128_f8f6f4 v[82:85], v[2:9], v[198:205], v[82:85]
	v_mfma_f32_16x16x128_f8f6f4 v[74:77], v[10:17], v[198:205], v[74:77]
	v_mfma_f32_16x16x128_f8f6f4 v[66:69], v[2:9], v[206:213], v[66:69]
	v_mfma_f32_16x16x128_f8f6f4 v[58:61], v[10:17], v[206:213], v[58:61]
	v_mfma_f32_16x16x128_f8f6f4 v[50:53], v[2:9], v[214:221], v[50:53]
	v_mfma_f32_16x16x128_f8f6f4 v[42:45], v[10:17], v[214:221], v[42:45]
	s_setprio 0
	s_setprio 1
	v_mfma_f32_16x16x128_f8f6f4 v[86:89], v[18:25], v[190:197], v[86:89]
	v_mfma_f32_16x16x128_f8f6f4 v[78:81], v[26:33], v[190:197], v[78:81]
	v_mfma_f32_16x16x128_f8f6f4 v[70:73], v[18:25], v[198:205], v[70:73]
	v_mfma_f32_16x16x128_f8f6f4 v[62:65], v[26:33], v[198:205], v[62:65]
	v_mfma_f32_16x16x128_f8f6f4 v[54:57], v[18:25], v[206:213], v[54:57]
	v_mfma_f32_16x16x128_f8f6f4 v[46:49], v[26:33], v[206:213], v[46:49]
	v_mfma_f32_16x16x128_f8f6f4 v[38:41], v[18:25], v[214:221], v[38:41]
	v_mfma_f32_16x16x128_f8f6f4 v[34:37], v[26:33], v[214:221], v[34:37]
	s_setprio 0
	s_add_i32 s71, s71, 2
	s_add_u32 s34, s34, 0x100
	s_addc_u32 s35, s35, 0
	s_cmp_gt_u32 s71, 53
	v_lshl_add_u64 v[172:173], v[172:173], 0, s[18:19]
	s_barrier
	s_cbranch_scc0 .LBB0_2259
	s_nop 15
	s_nop 15
	s_nop 15
	s_nop 15
	s_and_b64 vcc, exec, s[16:17]
	s_cbranch_vccz .LBB0_2262
	s_barrier
